# ssd chunk-state unit: conv weights/bias staged in LDS for 9 of 12 channel blocks (block waits no longer include the preceding global store)
# speedup vs baseline: 1.0226x; 1.0226x over previous
; DI void ssd_local_unit(Frame& F, int l, int ch, int g) {
;     ...
;     auto load_part = [&](const int part, v4u (&raw)[4][4]) {
; #pragma unroll
;         for (int cc = 0; cc < 4; ++cc)
; #pragma unroll
;             for (int j = 0; j < 4; ++j) raw[cc][j] = *(const v4u*)(proj + (size_t)(t0 + spc[j]) * PP + O_XBC + part * 256 + g * 128 + cg * 32 + cc * 8); };
;     ...
;     v4u ra[4][4], rb[4][4];
;     load_part(1, ra);
;     ssd_vectors(F, l, t0, g, DT, AC, RED);
;     load_part(2, rb);
;     do_part(1, ra);
.LBB0_838:
	v_cndmask_b32_e64 v136, 0, 1.0, s[4:5]
	s_add_i32 s4, s19, 0x11000
	s_mul_i32 s0, s28, 0x3000
	s_add_u32 s0, s45, s0
	s_mul_hi_i32 s1, s28, 0x3000
	v_cndmask_b32_e64 v138, 0, 1.0, s[2:3]
	s_addc_u32 s1, s43, s1
	s_mul_i32 s2, s28, 0xc00
	s_add_u32 s2, s42, s2
	s_mul_hi_i32 s3, s28, 0xc00
	v_lshlrev_b32_e32 v141, 5, v137
	s_addc_u32 s3, s44, s3
	s_lshl_b32 s52, s40, 1
	v_lshl_add_u64 v[52:53], v[52:53], 0, s[52:53]
	v_lshlrev_b32_e32 v66, 1, v141
	v_mov_b32_e32 v67, v3
	v_cndmask_b32_e64 v140, 0, 1.0, vcc
	v_cmp_lt_i32_e32 vcc, s30, v1
	v_lshl_add_u64 v[52:53], v[52:53], 0, v[66:67]
	v_lshl_add_u64 v[58:59], v[52:53], 0, s[84:85]
	v_cndmask_b32_e64 v134, 0, 1.0, vcc
	v_add_co_u32_e32 v52, vcc, s64, v52
	v_lshl_add_u64 v[56:57], v[56:57], 0, s[52:53]
	s_nop 0
	v_addc_co_u32_e32 v53, vcc, 0, v53, vcc
	v_lshl_add_u64 v[56:57], v[56:57], 0, v[66:67]
	v_lshl_add_u64 v[62:63], v[56:57], 0, s[84:85]
	v_add_co_u32_e32 v56, vcc, s64, v56
	v_lshl_add_u64 v[60:61], v[60:61], 0, s[52:53]
	s_nop 0
	v_addc_co_u32_e32 v57, vcc, 0, v57, vcc
	v_lshl_add_u64 v[60:61], v[60:61], 0, v[66:67]
	v_lshl_add_u64 v[80:81], v[60:61], 0, s[84:85]
	v_add_co_u32_e32 v60, vcc, s64, v60
	v_lshl_add_u64 v[64:65], v[64:65], 0, s[52:53]
	s_nop 0
	v_addc_co_u32_e32 v61, vcc, 0, v61, vcc
	v_lshl_add_u64 v[64:65], v[64:65], 0, v[66:67]
	v_or_b32_e32 v152, s40, v141
	v_mov_b32_e32 v153, v3
	v_lshl_add_u64 v[96:97], v[64:65], 0, s[84:85]
	v_add_co_u32_e32 v64, vcc, s64, v64
	v_lshlrev_b64 v[142:143], 2, v[152:153]
	s_nop 0
	v_addc_co_u32_e32 v65, vcc, 0, v65, vcc
	v_lshl_add_u64 v[144:145], s[0:1], 0, v[142:143]
	v_lshl_add_u64 v[146:147], s[2:3], 0, v[142:143]
	s_mov_b64 s[6:7], 0x400
	v_add_co_u32_e32 v148, vcc, s64, v144
	s_mov_b64 s[94:95], vcc
	v_cmp_gt_u32_e32 vcc, 0x1e0, v132
	s_and_saveexec_b64 s[92:93], vcc
	v_lshrrev_b32_e32 v202, 5, v132
	v_and_b32_e32 v203, 31, v132
	v_mul_u32_u24_e32 v204, 11, v202
	v_lshrrev_b32_e32 v204, 5, v204
	v_mul_u32_u24_e32 v205, 3, v204
	v_sub_u32_e32 v205, v202, v205
	v_mul_u32_u24_e32 v206, 0xc00, v204
	v_cmp_eq_u32_e32 vcc, 4, v204
	s_nop 1
	v_cndmask_b32_e32 v206, v206, v3, vcc
	v_lshl_add_u32 v206, v205, 10, v206
	v_lshl_add_u32 v206, v203, 4, v206
	s_lshl_b32 s72, s40, 2
	v_add_u32_e32 v206, s72, v206
	v_mov_b32_e32 v208, s0
	v_mov_b32_e32 v207, s2
	v_cndmask_b32_e32 v208, v208, v207, vcc
	v_mov_b32_e32 v209, s1
	v_mov_b32_e32 v207, s3
	v_cndmask_b32_e32 v209, v209, v207, vcc
	v_add_co_u32_e32 v208, vcc, v208, v206
	s_nop 1
	v_addc_co_u32_e32 v209, vcc, 0, v209, vcc
	global_load_dwordx4 v[210:213], v[208:209], off
	v_lshl_add_u32 v214, v132, 4, s19
	v_add_u32_e32 v214, 0x1b000, v214
	s_waitcnt vmcnt(0)
	ds_write_b128 v214, v[210:213]
	s_or_b64 exec, exec, s[92:93]
	v_lshl_add_u32 v215, v137, 7, s19
	v_add_u32_e32 v215, 0x1b000, v215
	s_mov_b64 vcc, s[94:95]
	s_waitcnt lgkmcnt(0)
	s_barrier
	global_load_dwordx4 v[100:103], v[52:53], off
	s_nop 0
	global_load_dwordx4 v[52:55], v[58:59], off offset:48
	global_load_dwordx4 v[68:71], v[58:59], off offset:32
	global_load_dwordx4 v[84:87], v[58:59], off offset:16
	global_load_dwordx4 v[104:107], v[56:57], off
	s_nop 0
	global_load_dwordx4 v[56:59], v[62:63], off offset:48
	global_load_dwordx4 v[72:75], v[62:63], off offset:32
	global_load_dwordx4 v[88:91], v[62:63], off offset:16
	global_load_dwordx4 v[108:111], v[60:61], off
	s_nop 0
	global_load_dwordx4 v[60:63], v[80:81], off offset:48
	global_load_dwordx4 v[76:79], v[80:81], off offset:32
	global_load_dwordx4 v[92:95], v[80:81], off offset:16
	global_load_dwordx4 v[112:115], v[64:65], off
	s_nop 0
	global_load_dwordx4 v[64:67], v[96:97], off offset:48
	global_load_dwordx4 v[80:83], v[96:97], off offset:32
	s_nop 0
	global_load_dwordx4 v[96:99], v[96:97], off offset:16
	s_nop 0
	ds_read_b128 v[162:165], v215 offset:6672
	ds_read_b128 v[166:169], v215 offset:6656
	v_lshl_add_u64 v[142:143], v[144:145], 0, s[6:7]
	ds_read_b128 v[170:173], v215 offset:528
	ds_read_b128 v[174:177], v215 offset:512
	ds_read_b128 v[178:181], v215 offset:2064
	ds_read_b128 v[182:185], v215 offset:2048
	v_addc_co_u32_e32 v149, vcc, 0, v145, vcc
	s_movk_i32 s42, 0x2000
	s_mov_b64 s[6:7], 0x1c00
	v_add_co_u32_e32 v150, vcc, s42, v144
	v_lshl_add_u64 v[142:143], v[144:145], 0, s[6:7]
	ds_read_b128 v[186:189], v215 offset:3584
	ds_read_b128 v[190:193], v215 offset:3600
	s_mov_b64 s[6:7], 0x2800
	v_addc_co_u32_e32 v151, vcc, 0, v145, vcc
	v_lshl_add_u64 v[142:143], v[144:145], 0, s[6:7]
	ds_read_b128 v[194:197], v215 offset:5120
	ds_read_b128 v[198:201], v215 offset:5136
	s_waitcnt vmcnt(16) lgkmcnt(0)
; __device__ __forceinline__ unsigned f2bf(float f) { unsigned u = __builtin_bit_cast(unsigned, f); return (u + 0x7fffu + ((u >> 16) & 1u)) >> 16; }
; DI unsigned pk2h(float lo, float hi) { const f32x2h_t v = {lo, hi}; return __builtin_bit_cast(unsigned, __builtin_convertvector(v, bf16x2h_t)); }
; DI float silu_f(float x) { return x * __builtin_amdgcn_rcpf(1.f + __expf(-x)); }
; DI void ssd_local_unit(Frame& F, int l, int ch, int g) {
;     ...
;         for (int cc = 0; cc < 4; ++cc) {
;             const int lc = cg * 32 + cc * 8, c0 = part * 256 + g * 128 + lc;
;             float acc[8];
;             { const f32x4 b0 = *(const f32x4*)(cb + c0), b1 = *(const f32x4*)(cb + c0 + 4);
; #pragma unroll
;               for (int e = 0; e < 4; ++e) { acc[e] = b0[e]; acc[4 + e] = b1[e]; } }
; #pragma unroll
;             for (int j = 0; j < 4; ++j) { float x[8]; unpack8(raw[cc][j], x);
;                 const f32x4 w0 = *(const f32x4*)(cw + j * XC + c0), w1 = *(const f32x4*)(cw + j * XC + c0 + 4);
; #pragma unroll
;                 for (int e = 0; e < 4; ++e) { acc[e] += w0[e] * okm[j] * x[e]; acc[4 + e] += w1[e] * okm[j] * x[4 + e]; } }
; #pragma unroll
;             for (int e = 0; e < 8; ++e) acc[e] = silu_f(acc[e]);
;             v4u o; o.x = pk2h(acc[0], acc[1]); o.y = pk2h(acc[2], acc[3]); o.z = pk2h(acc[4], acc[5]); o.w = pk2h(acc[6], acc[7]);
;             *(v4u*)(xbcc + (size_t)(t0 + s) * XC + c0) = o;
;             if (part == 0) { const int r2 = lc >> 6; const float dtv = DT[r2 * 128 + s], sc = dtv * __expf(AC[r2 * 128 + 127] - AC[r2 * 128 + s]);
; #pragma unroll
;                 for (int e = 0; e < 8; ++e) { XWT[(lc + e) * LP + s] = (bf16)f2bf(acc[e] * sc); XD[(lc + e) * LP + s] = (bf16)f2bf(acc[e] * dtv); } }
;             else if (part == 1) {
; #pragma unroll
;                 for (int e = 0; e < 8; ++e) BT[(lc + e) * LP + s] = (bf16)f2bf(acc[e]); }
	v_lshlrev_b32_e32 v142, 16, v116
	v_and_b32_e32 v143, 0xffff0000, v116
	v_lshlrev_b32_e32 v116, 16, v117
	v_and_b32_e32 v117, 0xffff0000, v117
	s_movk_i32 s5, 0x2200
	s_nop 0
	v_pk_mul_f32 v[174:175], v[140:141], v[174:175] op_sel_hi:[0,1]
	v_pk_fma_f32 v[142:143], v[174:175], v[142:143], v[166:167]
	v_lshlrev_b32_e32 v166, 16, v120
	v_and_b32_e32 v167, 0xffff0000, v120
	s_nop 0
	v_pk_mul_f32 v[174:175], v[138:139], v[182:183] op_sel_hi:[0,1]
	v_pk_fma_f32 v[142:143], v[174:175], v[166:167], v[142:143]
	v_lshlrev_b32_e32 v166, 16, v124
	v_and_b32_e32 v167, 0xffff0000, v124
	v_lshlrev_b32_e32 v120, 16, v121
	s_nop 0
	v_pk_mul_f32 v[174:175], v[136:137], v[186:187] op_sel_hi:[0,1]
	v_pk_fma_f32 v[142:143], v[174:175], v[166:167], v[142:143]
	v_lshlrev_b32_e32 v166, 16, v128
	v_and_b32_e32 v167, 0xffff0000, v128
	v_and_b32_e32 v121, 0xffff0000, v121
	s_nop 0
	v_pk_mul_f32 v[174:175], v[134:135], v[194:195] op_sel_hi:[0,1]
	v_pk_fma_f32 v[142:143], v[174:175], v[166:167], v[142:143]
	s_nop 0
	v_mul_f32_e32 v0, 0xbfb8aa3b, v142
	v_exp_f32_e32 v0, v0
	s_nop 0
	v_add_f32_e32 v0, 1.0, v0
	v_rcp_f32_e32 v166, v0
	v_mul_f32_e32 v0, 0xbfb8aa3b, v143
	v_exp_f32_e32 v0, v0
	s_nop 0
	v_add_f32_e32 v0, 1.0, v0
	v_rcp_f32_e32 v167, v0
	s_nop 0
	v_pk_mul_f32 v[166:167], v[142:143], v[166:167]
	v_pk_mul_f32 v[142:143], v[140:141], v[176:177] op_sel_hi:[0,1]
	v_pk_fma_f32 v[116:117], v[142:143], v[116:117], v[168:169]
	v_pk_mul_f32 v[142:143], v[138:139], v[184:185] op_sel_hi:[0,1]
	v_pk_fma_f32 v[116:117], v[142:143], v[120:121], v[116:117]
	v_lshlrev_b32_e32 v120, 16, v125
	v_and_b32_e32 v121, 0xffff0000, v125
	v_pk_mul_f32 v[124:125], v[136:137], v[188:189] op_sel_hi:[0,1]
	v_pk_fma_f32 v[116:117], v[124:125], v[120:121], v[116:117]
	v_lshlrev_b32_e32 v120, 16, v129
	v_and_b32_e32 v121, 0xffff0000, v129
	v_pk_mul_f32 v[124:125], v[134:135], v[196:197] op_sel_hi:[0,1]
	v_pk_fma_f32 v[116:117], v[124:125], v[120:121], v[116:117]
	v_pk_mul_f32 v[124:125], v[140:141], v[170:171] op_sel_hi:[0,1]
	v_mul_f32_e32 v0, 0xbfb8aa3b, v116
	v_exp_f32_e32 v0, v0
	v_pk_mul_f32 v[128:129], v[138:139], v[178:179] op_sel_hi:[0,1]
	v_add_f32_e32 v0, 1.0, v0
	v_rcp_f32_e32 v120, v0
	v_mul_f32_e32 v0, 0xbfb8aa3b, v117
	v_exp_f32_e32 v0, v0
	s_nop 0
	v_add_f32_e32 v0, 1.0, v0
	v_rcp_f32_e32 v121, v0
	s_nop 0
	v_pk_mul_f32 v[120:121], v[116:117], v[120:121]
	v_lshlrev_b32_e32 v116, 16, v118
	v_and_b32_e32 v117, 0xffff0000, v118
	v_pk_fma_f32 v[116:117], v[124:125], v[116:117], v[162:163]
	v_lshlrev_b32_e32 v124, 16, v122
	v_and_b32_e32 v125, 0xffff0000, v122
	v_pk_fma_f32 v[116:117], v[128:129], v[124:125], v[116:117]
	v_lshlrev_b32_e32 v124, 16, v126
	v_and_b32_e32 v125, 0xffff0000, v126
	v_pk_mul_f32 v[128:129], v[136:137], v[190:191] op_sel_hi:[0,1]
	v_pk_fma_f32 v[116:117], v[128:129], v[124:125], v[116:117]
	v_lshlrev_b32_e32 v124, 16, v130
	v_and_b32_e32 v125, 0xffff0000, v130
	s_waitcnt vmcnt(0)
	v_pk_mul_f32 v[128:129], v[134:135], v[198:199] op_sel_hi:[0,1]
	v_pk_fma_f32 v[116:117], v[128:129], v[124:125], v[116:117]
	v_or_b32_e32 v163, 8, v141
	v_mul_f32_e32 v0, 0xbfb8aa3b, v116
	v_exp_f32_e32 v0, v0
	v_or_b32_e32 v162, 16, v141
	v_lshlrev_b32_e32 v198, 16, v100
	v_and_b32_e32 v199, 0xffff0000, v100
	v_add_f32_e32 v0, 1.0, v0
	v_rcp_f32_e32 v124, v0
	v_mul_f32_e32 v0, 0xbfb8aa3b, v117
	v_exp_f32_e32 v0, v0
	v_lshlrev_b32_e32 v100, 16, v101
	v_and_b32_e32 v101, 0xffff0000, v101
	v_add_f32_e32 v0, 1.0, v0
	v_rcp_f32_e32 v125, v0
	s_nop 0
	v_pk_mul_f32 v[124:125], v[116:117], v[124:125]
	v_lshlrev_b32_e32 v116, 16, v119
	v_and_b32_e32 v117, 0xffff0000, v119
	v_pk_mul_f32 v[118:119], v[140:141], v[172:173] op_sel_hi:[0,1]
	v_pk_fma_f32 v[116:117], v[118:119], v[116:117], v[164:165]
	v_lshlrev_b32_e32 v118, 16, v123
	v_and_b32_e32 v119, 0xffff0000, v123
	v_pk_mul_f32 v[122:123], v[138:139], v[180:181] op_sel_hi:[0,1]
	v_pk_fma_f32 v[116:117], v[122:123], v[118:119], v[116:117]
	v_lshlrev_b32_e32 v118, 16, v127
	v_and_b32_e32 v119, 0xffff0000, v127
	v_pk_mul_f32 v[122:123], v[136:137], v[192:193] op_sel_hi:[0,1]
	v_pk_fma_f32 v[116:117], v[122:123], v[118:119], v[116:117]
	v_lshlrev_b32_e32 v118, 16, v131
	v_and_b32_e32 v119, 0xffff0000, v131
	v_pk_mul_f32 v[122:123], v[134:135], v[200:201] op_sel_hi:[0,1]
	v_pk_fma_f32 v[116:117], v[122:123], v[118:119], v[116:117]
	v_mov_b64_e32 v[126:127], s[20:21]
	v_mul_f32_e32 v0, 0xbfb8aa3b, v116
	v_exp_f32_e32 v0, v0
	v_mad_i64_i32 v[126:127], s[6:7], v135, s65, v[126:127]
	s_mov_b64 s[6:7], 0x1c100000
	v_add_f32_e32 v0, 1.0, v0
	v_rcp_f32_e32 v118, v0
	v_mul_f32_e32 v0, 0xbfb8aa3b, v117
	v_exp_f32_e32 v0, v0
	v_lshl_add_u64 v[142:143], v[126:127], 0, s[6:7]
	v_lshlrev_b32_e32 v126, 1, v152
	v_mov_b32_e32 v127, v3
	v_add_f32_e32 v0, 1.0, v0
	v_rcp_f32_e32 v119, v0
	v_lshlrev_b32_e32 v164, 1, v1
	v_lshl_add_u64 v[152:153], v[142:143], 0, v[126:127]
	v_add_u32_e32 v135, s19, v164
	v_pk_mul_f32 v[122:123], v[116:117], v[118:119]
	v_cvt_pk_bf16_f32 v116, v166, v167
	v_cvt_pk_bf16_f32 v117, v120, v121
	v_cvt_pk_bf16_f32 v118, v124, v125
	v_cvt_pk_bf16_f32 v119, v122, v123
	v_bfe_u32 v0, v166, 16, 1
	global_store_dwordx4 v[152:153], v[116:119], off offset:512
	v_add3_u32 v0, v166, v0, s97
	s_mov_b64 s[6:7], 0x420
	v_mad_u32_u24 v116, v137, s5, v135
	ds_write_b16_d16_hi v116, v0 offset:34816
	v_bfe_u32 v0, v167, 16, 1
	v_add3_u32 v0, v167, v0, s97
	ds_write_b16_d16_hi v116, v0 offset:35088
	v_bfe_u32 v0, v120, 16, 1
	v_add3_u32 v0, v120, v0, s97
	ds_write_b16_d16_hi v116, v0 offset:35360
	v_bfe_u32 v0, v121, 16, 1
	v_add3_u32 v0, v121, v0, s97
	ds_write_b16_d16_hi v116, v0 offset:35632
	v_bfe_u32 v0, v124, 16, 1
	v_add3_u32 v0, v124, v0, s97
	ds_write_b16_d16_hi v116, v0 offset:35904
	v_bfe_u32 v0, v125, 16, 1
	v_add3_u32 v0, v125, v0, s97
	ds_write_b16_d16_hi v116, v0 offset:36176
	v_bfe_u32 v0, v122, 16, 1
	v_add3_u32 v0, v122, v0, s97
	ds_write_b16_d16_hi v116, v0 offset:36448
	v_bfe_u32 v0, v123, 16, 1
	v_add3_u32 v0, v123, v0, s97
	ds_write_b16_d16_hi v116, v0 offset:36720
	ds_read_b128 v[118:121], v215 offset:6704
	ds_read_b128 v[122:125], v215 offset:6688
	v_lshl_add_u64 v[130:131], v[144:145], 0, s[6:7]
	ds_read_b128 v[126:129], v215 offset:560
	ds_read_b128 v[166:169], v215 offset:544
	ds_read_b128 v[170:173], v215 offset:2096
	ds_read_b128 v[174:177], v215 offset:2080
	s_mov_b64 s[6:7], 0x1c20
	v_lshl_add_u64 v[130:131], v[144:145], 0, s[6:7]
	ds_read_b128 v[178:181], v215 offset:3616
	ds_read_b128 v[182:185], v215 offset:3632
	s_mov_b64 s[6:7], 0x2820
	v_lshl_add_u64 v[130:131], v[144:145], 0, s[6:7]
	ds_read_b128 v[186:189], v215 offset:5152
	ds_read_b128 v[190:193], v215 offset:5168
	v_lshlrev_b32_e32 v130, 16, v36
	v_and_b32_e32 v131, 0xffff0000, v36
	v_lshlrev_b32_e32 v36, 16, v37
	v_and_b32_e32 v37, 0xffff0000, v37
	s_mov_b64 s[6:7], 0x440
	s_waitcnt lgkmcnt(0)
; __device__ __forceinline__ unsigned f2bf(float f) { unsigned u = __builtin_bit_cast(unsigned, f); return (u + 0x7fffu + ((u >> 16) & 1u)) >> 16; }
; DI unsigned pk2h(float lo, float hi) { const f32x2h_t v = {lo, hi}; return __builtin_bit_cast(unsigned, __builtin_convertvector(v, bf16x2h_t)); }
; DI float silu_f(float x) { return x * __builtin_amdgcn_rcpf(1.f + __expf(-x)); }
; DI void ssd_local_unit(Frame& F, int l, int ch, int g) {
;     ...
;         for (int cc = 0; cc < 4; ++cc) {
;             const int lc = cg * 32 + cc * 8, c0 = part * 256 + g * 128 + lc;
;             float acc[8];
;             { const f32x4 b0 = *(const f32x4*)(cb + c0), b1 = *(const f32x4*)(cb + c0 + 4);
; #pragma unroll
;               for (int e = 0; e < 4; ++e) { acc[e] = b0[e]; acc[4 + e] = b1[e]; } }
; #pragma unroll
;             for (int j = 0; j < 4; ++j) { float x[8]; unpack8(raw[cc][j], x);
;                 const f32x4 w0 = *(const f32x4*)(cw + j * XC + c0), w1 = *(const f32x4*)(cw + j * XC + c0 + 4);
; #pragma unroll
;                 for (int e = 0; e < 4; ++e) { acc[e] += w0[e] * okm[j] * x[e]; acc[4 + e] += w1[e] * okm[j] * x[4 + e]; } }
; #pragma unroll
;             for (int e = 0; e < 8; ++e) acc[e] = silu_f(acc[e]);
;             v4u o; o.x = pk2h(acc[0], acc[1]); o.y = pk2h(acc[2], acc[3]); o.z = pk2h(acc[4], acc[5]); o.w = pk2h(acc[6], acc[7]);
;             *(v4u*)(xbcc + (size_t)(t0 + s) * XC + c0) = o;
;             if (part == 0) { const int r2 = lc >> 6; const float dtv = DT[r2 * 128 + s], sc = dtv * __expf(AC[r2 * 128 + 127] - AC[r2 * 128 + s]);
; #pragma unroll
;                 for (int e = 0; e < 8; ++e) { XWT[(lc + e) * LP + s] = (bf16)f2bf(acc[e] * sc); XD[(lc + e) * LP + s] = (bf16)f2bf(acc[e] * dtv); } }
;             else if (part == 1) {
; #pragma unroll
;                 for (int e = 0; e < 8; ++e) BT[(lc + e) * LP + s] = (bf16)f2bf(acc[e]); }
	v_pk_mul_f32 v[166:167], v[140:141], v[166:167] op_sel_hi:[0,1]
	v_pk_fma_f32 v[122:123], v[166:167], v[130:131], v[122:123]
	v_lshlrev_b32_e32 v130, 16, v40
	v_and_b32_e32 v131, 0xffff0000, v40
	s_nop 0
	v_pk_mul_f32 v[166:167], v[138:139], v[174:175] op_sel_hi:[0,1]
	v_pk_fma_f32 v[122:123], v[166:167], v[130:131], v[122:123]
	v_lshlrev_b32_e32 v130, 16, v44
	v_and_b32_e32 v131, 0xffff0000, v44
	s_nop 0
	v_pk_mul_f32 v[166:167], v[136:137], v[178:179] op_sel_hi:[0,1]
	v_pk_fma_f32 v[122:123], v[166:167], v[130:131], v[122:123]
	v_lshlrev_b32_e32 v130, 16, v48
	v_and_b32_e32 v131, 0xffff0000, v48
	s_nop 0
	v_pk_mul_f32 v[166:167], v[134:135], v[186:187] op_sel_hi:[0,1]
	v_pk_fma_f32 v[122:123], v[166:167], v[130:131], v[122:123]
	v_lshlrev_b32_e32 v40, 16, v41
	v_mul_f32_e32 v0, 0xbfb8aa3b, v122
	v_exp_f32_e32 v0, v0
	v_and_b32_e32 v41, 0xffff0000, v41
	v_add_f32_e32 v0, 1.0, v0
	v_rcp_f32_e32 v130, v0
	v_mul_f32_e32 v0, 0xbfb8aa3b, v123
	v_exp_f32_e32 v0, v0
	s_nop 0
	v_add_f32_e32 v0, 1.0, v0
	v_rcp_f32_e32 v131, v0
	s_nop 0
	v_pk_mul_f32 v[122:123], v[122:123], v[130:131]
	v_pk_mul_f32 v[130:131], v[140:141], v[168:169] op_sel_hi:[0,1]
	v_pk_fma_f32 v[36:37], v[130:131], v[36:37], v[124:125]
	v_pk_mul_f32 v[124:125], v[138:139], v[176:177] op_sel_hi:[0,1]
	v_pk_fma_f32 v[36:37], v[124:125], v[40:41], v[36:37]
	v_lshlrev_b32_e32 v40, 16, v45
	v_and_b32_e32 v41, 0xffff0000, v45
	v_pk_mul_f32 v[44:45], v[136:137], v[180:181] op_sel_hi:[0,1]
	v_pk_fma_f32 v[36:37], v[44:45], v[40:41], v[36:37]
	v_lshlrev_b32_e32 v40, 16, v49
	v_and_b32_e32 v41, 0xffff0000, v49
	v_pk_mul_f32 v[44:45], v[134:135], v[188:189] op_sel_hi:[0,1]
	v_pk_fma_f32 v[36:37], v[44:45], v[40:41], v[36:37]
	v_pk_mul_f32 v[44:45], v[140:141], v[126:127] op_sel_hi:[0,1]
	v_mul_f32_e32 v0, 0xbfb8aa3b, v36
	v_exp_f32_e32 v0, v0
	v_pk_mul_f32 v[48:49], v[138:139], v[170:171] op_sel_hi:[0,1]
	v_add_f32_e32 v0, 1.0, v0
	v_rcp_f32_e32 v40, v0
	v_mul_f32_e32 v0, 0xbfb8aa3b, v37
	v_exp_f32_e32 v0, v0
	s_nop 0
	v_add_f32_e32 v0, 1.0, v0
	v_rcp_f32_e32 v41, v0
	s_nop 0
	v_pk_mul_f32 v[40:41], v[36:37], v[40:41]
	v_lshlrev_b32_e32 v36, 16, v38
	v_and_b32_e32 v37, 0xffff0000, v38
	v_pk_fma_f32 v[36:37], v[44:45], v[36:37], v[118:119]
	v_lshlrev_b32_e32 v44, 16, v42
	v_and_b32_e32 v45, 0xffff0000, v42
	v_pk_fma_f32 v[36:37], v[48:49], v[44:45], v[36:37]
	v_lshlrev_b32_e32 v44, 16, v46
	v_and_b32_e32 v45, 0xffff0000, v46
	v_pk_mul_f32 v[48:49], v[136:137], v[182:183] op_sel_hi:[0,1]
	v_pk_fma_f32 v[36:37], v[48:49], v[44:45], v[36:37]
	v_lshlrev_b32_e32 v44, 16, v50
	v_and_b32_e32 v45, 0xffff0000, v50
	s_nop 0
	v_pk_mul_f32 v[48:49], v[134:135], v[190:191] op_sel_hi:[0,1]
	v_pk_fma_f32 v[36:37], v[48:49], v[44:45], v[36:37]
	s_nop 0
	v_mul_f32_e32 v0, 0xbfb8aa3b, v36
	v_exp_f32_e32 v0, v0
	s_nop 0
	v_add_f32_e32 v0, 1.0, v0
	v_rcp_f32_e32 v44, v0
	v_mul_f32_e32 v0, 0xbfb8aa3b, v37
	v_exp_f32_e32 v0, v0
	s_nop 0
	v_add_f32_e32 v0, 1.0, v0
	v_rcp_f32_e32 v45, v0
	s_nop 0
	v_pk_mul_f32 v[44:45], v[36:37], v[44:45]
	v_lshlrev_b32_e32 v36, 16, v39
	v_and_b32_e32 v37, 0xffff0000, v39
	v_pk_mul_f32 v[38:39], v[140:141], v[128:129] op_sel_hi:[0,1]
	v_pk_fma_f32 v[36:37], v[38:39], v[36:37], v[120:121]
	v_lshlrev_b32_e32 v38, 16, v43
	v_and_b32_e32 v39, 0xffff0000, v43
	v_pk_mul_f32 v[42:43], v[138:139], v[172:173] op_sel_hi:[0,1]
	v_pk_fma_f32 v[36:37], v[42:43], v[38:39], v[36:37]
	v_lshlrev_b32_e32 v38, 16, v47
	v_and_b32_e32 v39, 0xffff0000, v47
	v_pk_mul_f32 v[42:43], v[136:137], v[184:185] op_sel_hi:[0,1]
	v_pk_fma_f32 v[36:37], v[42:43], v[38:39], v[36:37]
	v_lshlrev_b32_e32 v38, 16, v51
	v_and_b32_e32 v39, 0xffff0000, v51
	v_pk_mul_f32 v[42:43], v[134:135], v[192:193] op_sel_hi:[0,1]
	v_pk_fma_f32 v[36:37], v[42:43], v[38:39], v[36:37]
	s_nop 0
	v_mul_f32_e32 v0, 0xbfb8aa3b, v36
	v_exp_f32_e32 v0, v0
	s_nop 0
	v_add_f32_e32 v0, 1.0, v0
	v_rcp_f32_e32 v38, v0
	v_mul_f32_e32 v0, 0xbfb8aa3b, v37
	v_exp_f32_e32 v0, v0
	s_nop 0
	v_add_f32_e32 v0, 1.0, v0
	v_rcp_f32_e32 v39, v0
	v_bfe_u32 v0, v122, 16, 1
	v_add3_u32 v0, v122, v0, s97
	v_pk_mul_f32 v[42:43], v[36:37], v[38:39]
	v_cvt_pk_bf16_f32 v36, v122, v123
	v_cvt_pk_bf16_f32 v37, v40, v41
	v_cvt_pk_bf16_f32 v38, v44, v45
	v_cvt_pk_bf16_f32 v39, v42, v43
	global_store_dwordx4 v[152:153], v[36:39], off offset:528
	s_nop 1
	v_mad_u32_u24 v36, v163, s66, v135
	ds_write_b16_d16_hi v36, v0 offset:34816
	v_bfe_u32 v0, v123, 16, 1
	v_add3_u32 v0, v123, v0, s97
	ds_write_b16_d16_hi v116, v0 offset:37264
	v_bfe_u32 v0, v40, 16, 1
	v_add3_u32 v0, v40, v0, s97
	ds_write_b16_d16_hi v116, v0 offset:37536
	v_bfe_u32 v0, v41, 16, 1
	v_add3_u32 v0, v41, v0, s97
	ds_write_b16_d16_hi v116, v0 offset:37808
	v_bfe_u32 v0, v44, 16, 1
	v_add3_u32 v0, v44, v0, s97
	ds_write_b16_d16_hi v116, v0 offset:38080
	v_bfe_u32 v0, v45, 16, 1
	v_add3_u32 v0, v45, v0, s97
	ds_write_b16_d16_hi v116, v0 offset:38352
	v_bfe_u32 v0, v42, 16, 1
	v_add3_u32 v0, v42, v0, s97
	ds_write_b16_d16_hi v116, v0 offset:38624
	v_bfe_u32 v0, v43, 16, 1
	v_add3_u32 v0, v43, v0, s97
	ds_write_b16_d16_hi v116, v0 offset:38896
	v_lshl_add_u64 v[122:123], v[144:145], 0, s[6:7]
	ds_read_b128 v[36:39], v215 offset:6736
	ds_read_b128 v[40:43], v215 offset:6720
	ds_read_b128 v[44:47], v215 offset:592
	ds_read_b128 v[48:51], v215 offset:576
	ds_read_b128 v[118:121], v215 offset:2128
	s_nop 0
	ds_read_b128 v[122:125], v215 offset:2112
	s_mov_b64 s[6:7], 0x1c40
	v_lshl_add_u64 v[130:131], v[144:145], 0, s[6:7]
	ds_read_b128 v[126:129], v215 offset:3648
	ds_read_b128 v[166:169], v215 offset:3664
	s_mov_b64 s[6:7], 0x2840
	v_lshl_add_u64 v[130:131], v[144:145], 0, s[6:7]
	ds_read_b128 v[170:173], v215 offset:5184
	ds_read_b128 v[174:177], v215 offset:5200
	v_lshlrev_b32_e32 v130, 16, v20
	v_and_b32_e32 v131, 0xffff0000, v20
	v_lshlrev_b32_e32 v20, 16, v21
	v_and_b32_e32 v21, 0xffff0000, v21
	s_mov_b64 s[6:7], 0x460
	s_waitcnt lgkmcnt(0)
; __device__ __forceinline__ unsigned f2bf(float f) { unsigned u = __builtin_bit_cast(unsigned, f); return (u + 0x7fffu + ((u >> 16) & 1u)) >> 16; }
; DI unsigned pk2h(float lo, float hi) { const f32x2h_t v = {lo, hi}; return __builtin_bit_cast(unsigned, __builtin_convertvector(v, bf16x2h_t)); }
; DI float silu_f(float x) { return x * __builtin_amdgcn_rcpf(1.f + __expf(-x)); }
; DI void ssd_local_unit(Frame& F, int l, int ch, int g) {
;     ...
;         for (int cc = 0; cc < 4; ++cc) {
;             const int lc = cg * 32 + cc * 8, c0 = part * 256 + g * 128 + lc;
;             float acc[8];
;             { const f32x4 b0 = *(const f32x4*)(cb + c0), b1 = *(const f32x4*)(cb + c0 + 4);
; #pragma unroll
;               for (int e = 0; e < 4; ++e) { acc[e] = b0[e]; acc[4 + e] = b1[e]; } }
; #pragma unroll
;             for (int j = 0; j < 4; ++j) { float x[8]; unpack8(raw[cc][j], x);
;                 const f32x4 w0 = *(const f32x4*)(cw + j * XC + c0), w1 = *(const f32x4*)(cw + j * XC + c0 + 4);
; #pragma unroll
;                 for (int e = 0; e < 4; ++e) { acc[e] += w0[e] * okm[j] * x[e]; acc[4 + e] += w1[e] * okm[j] * x[4 + e]; } }
; #pragma unroll
;             for (int e = 0; e < 8; ++e) acc[e] = silu_f(acc[e]);
;             v4u o; o.x = pk2h(acc[0], acc[1]); o.y = pk2h(acc[2], acc[3]); o.z = pk2h(acc[4], acc[5]); o.w = pk2h(acc[6], acc[7]);
;             *(v4u*)(xbcc + (size_t)(t0 + s) * XC + c0) = o;
;             if (part == 0) { const int r2 = lc >> 6; const float dtv = DT[r2 * 128 + s], sc = dtv * __expf(AC[r2 * 128 + 127] - AC[r2 * 128 + s]);
; #pragma unroll
;                 for (int e = 0; e < 8; ++e) { XWT[(lc + e) * LP + s] = (bf16)f2bf(acc[e] * sc); XD[(lc + e) * LP + s] = (bf16)f2bf(acc[e] * dtv); } }
;             else if (part == 1) {
; #pragma unroll
;                 for (int e = 0; e < 8; ++e) BT[(lc + e) * LP + s] = (bf16)f2bf(acc[e]); }
	v_pk_mul_f32 v[48:49], v[140:141], v[48:49] op_sel_hi:[0,1]
	v_pk_fma_f32 v[40:41], v[48:49], v[130:131], v[40:41]
	v_lshlrev_b32_e32 v48, 16, v24
	v_and_b32_e32 v49, 0xffff0000, v24
	s_nop 0
	v_pk_mul_f32 v[122:123], v[138:139], v[122:123] op_sel_hi:[0,1]
	v_pk_fma_f32 v[40:41], v[122:123], v[48:49], v[40:41]
	v_lshlrev_b32_e32 v48, 16, v28
	v_and_b32_e32 v49, 0xffff0000, v28
	s_nop 0
	v_pk_mul_f32 v[122:123], v[136:137], v[126:127] op_sel_hi:[0,1]
	v_pk_fma_f32 v[40:41], v[122:123], v[48:49], v[40:41]
	v_lshlrev_b32_e32 v48, 16, v32
	v_and_b32_e32 v49, 0xffff0000, v32
	s_nop 0
	v_pk_mul_f32 v[122:123], v[134:135], v[170:171] op_sel_hi:[0,1]
	v_pk_fma_f32 v[40:41], v[122:123], v[48:49], v[40:41]
	v_lshlrev_b32_e32 v24, 16, v25
	v_mul_f32_e32 v0, 0xbfb8aa3b, v40
	v_exp_f32_e32 v0, v0
	v_and_b32_e32 v25, 0xffff0000, v25
	v_lshlrev_b32_e32 v126, 16, v4
	v_and_b32_e32 v127, 0xffff0000, v4
	v_add_f32_e32 v0, 1.0, v0
	v_rcp_f32_e32 v48, v0
	v_mul_f32_e32 v0, 0xbfb8aa3b, v41
	v_exp_f32_e32 v0, v0
	v_lshlrev_b32_e32 v4, 16, v5
	v_and_b32_e32 v5, 0xffff0000, v5
	v_add_f32_e32 v0, 1.0, v0
	v_rcp_f32_e32 v49, v0
	s_nop 0
	v_pk_mul_f32 v[40:41], v[40:41], v[48:49]
	v_pk_mul_f32 v[48:49], v[140:141], v[50:51] op_sel_hi:[0,1]
	v_pk_fma_f32 v[20:21], v[48:49], v[20:21], v[42:43]
	v_pk_mul_f32 v[42:43], v[138:139], v[124:125] op_sel_hi:[0,1]
	v_pk_fma_f32 v[20:21], v[42:43], v[24:25], v[20:21]
	v_lshlrev_b32_e32 v24, 16, v29
	v_and_b32_e32 v25, 0xffff0000, v29
	v_pk_mul_f32 v[28:29], v[136:137], v[128:129] op_sel_hi:[0,1]
	v_pk_fma_f32 v[20:21], v[28:29], v[24:25], v[20:21]
	v_lshlrev_b32_e32 v24, 16, v33
	v_and_b32_e32 v25, 0xffff0000, v33
	v_pk_mul_f32 v[28:29], v[134:135], v[172:173] op_sel_hi:[0,1]
	v_pk_fma_f32 v[20:21], v[28:29], v[24:25], v[20:21]
	v_pk_mul_f32 v[28:29], v[140:141], v[44:45] op_sel_hi:[0,1]
	v_mul_f32_e32 v0, 0xbfb8aa3b, v20
	v_exp_f32_e32 v0, v0
	v_pk_mul_f32 v[32:33], v[138:139], v[118:119] op_sel_hi:[0,1]
	v_add_f32_e32 v0, 1.0, v0
	v_rcp_f32_e32 v24, v0
	v_mul_f32_e32 v0, 0xbfb8aa3b, v21
	v_exp_f32_e32 v0, v0
	s_nop 0
	v_add_f32_e32 v0, 1.0, v0
	v_rcp_f32_e32 v25, v0
	s_nop 0
	v_pk_mul_f32 v[24:25], v[20:21], v[24:25]
	v_lshlrev_b32_e32 v20, 16, v22
	v_and_b32_e32 v21, 0xffff0000, v22
	v_pk_fma_f32 v[20:21], v[28:29], v[20:21], v[36:37]
	v_lshlrev_b32_e32 v28, 16, v26
	v_and_b32_e32 v29, 0xffff0000, v26
	v_pk_fma_f32 v[20:21], v[32:33], v[28:29], v[20:21]
	v_lshlrev_b32_e32 v28, 16, v30
	v_and_b32_e32 v29, 0xffff0000, v30
	v_pk_mul_f32 v[32:33], v[136:137], v[166:167] op_sel_hi:[0,1]
	v_pk_fma_f32 v[20:21], v[32:33], v[28:29], v[20:21]
	v_lshlrev_b32_e32 v28, 16, v34
	v_and_b32_e32 v29, 0xffff0000, v34
	s_nop 0
	v_pk_mul_f32 v[32:33], v[134:135], v[174:175] op_sel_hi:[0,1]
	v_pk_fma_f32 v[20:21], v[32:33], v[28:29], v[20:21]
	s_nop 0
	v_mul_f32_e32 v0, 0xbfb8aa3b, v20
	v_exp_f32_e32 v0, v0
	s_nop 0
	v_add_f32_e32 v0, 1.0, v0
	v_rcp_f32_e32 v28, v0
	v_mul_f32_e32 v0, 0xbfb8aa3b, v21
	v_exp_f32_e32 v0, v0
	s_nop 0
	v_add_f32_e32 v0, 1.0, v0
	v_rcp_f32_e32 v29, v0
	s_nop 0
	v_pk_mul_f32 v[28:29], v[20:21], v[28:29]
	v_lshlrev_b32_e32 v20, 16, v23
	v_and_b32_e32 v21, 0xffff0000, v23
	v_pk_mul_f32 v[22:23], v[140:141], v[46:47] op_sel_hi:[0,1]
	v_pk_fma_f32 v[20:21], v[22:23], v[20:21], v[38:39]
	v_lshlrev_b32_e32 v22, 16, v27
	v_and_b32_e32 v23, 0xffff0000, v27
	v_pk_mul_f32 v[26:27], v[138:139], v[120:121] op_sel_hi:[0,1]
	v_pk_fma_f32 v[20:21], v[26:27], v[22:23], v[20:21]
	v_lshlrev_b32_e32 v22, 16, v31
	v_and_b32_e32 v23, 0xffff0000, v31
	v_pk_mul_f32 v[26:27], v[136:137], v[168:169] op_sel_hi:[0,1]
	v_pk_fma_f32 v[20:21], v[26:27], v[22:23], v[20:21]
	v_lshlrev_b32_e32 v22, 16, v35
	v_and_b32_e32 v23, 0xffff0000, v35
	v_pk_mul_f32 v[26:27], v[134:135], v[176:177] op_sel_hi:[0,1]
	v_pk_fma_f32 v[20:21], v[26:27], v[22:23], v[20:21]
	v_or_b32_e32 v139, 24, v141
	v_mul_f32_e32 v0, 0xbfb8aa3b, v20
	v_exp_f32_e32 v0, v0
	s_nop 0
	v_add_f32_e32 v0, 1.0, v0
	v_rcp_f32_e32 v22, v0
	v_mul_f32_e32 v0, 0xbfb8aa3b, v21
	v_exp_f32_e32 v0, v0
	s_nop 0
	v_add_f32_e32 v0, 1.0, v0
	v_rcp_f32_e32 v23, v0
	v_bfe_u32 v0, v40, 16, 1
	v_add3_u32 v0, v40, v0, s97
	v_pk_mul_f32 v[26:27], v[20:21], v[22:23]
	v_cvt_pk_bf16_f32 v20, v40, v41
	v_cvt_pk_bf16_f32 v21, v24, v25
	v_cvt_pk_bf16_f32 v22, v28, v29
	v_cvt_pk_bf16_f32 v23, v26, v27
	global_store_dwordx4 v[152:153], v[20:23], off offset:544
	s_nop 1
	v_mad_u32_u24 v20, v162, s66, v135
	ds_write_b16_d16_hi v20, v0 offset:34816
	v_bfe_u32 v0, v41, 16, 1
	v_add3_u32 v0, v41, v0, s97
	ds_write_b16_d16_hi v116, v0 offset:39440
	v_bfe_u32 v0, v24, 16, 1
	v_add3_u32 v0, v24, v0, s97
	ds_write_b16_d16_hi v116, v0 offset:39712
	v_bfe_u32 v0, v25, 16, 1
	v_add3_u32 v0, v25, v0, s97
	ds_write_b16_d16_hi v116, v0 offset:39984
	v_bfe_u32 v0, v28, 16, 1
	v_add3_u32 v0, v28, v0, s97
	ds_write_b16_d16_hi v116, v0 offset:40256
	v_bfe_u32 v0, v29, 16, 1
	v_add3_u32 v0, v29, v0, s97
	ds_write_b16_d16_hi v116, v0 offset:40528
	v_bfe_u32 v0, v26, 16, 1
	v_add3_u32 v0, v26, v0, s97
	ds_write_b16_d16_hi v116, v0 offset:40800
	v_bfe_u32 v0, v27, 16, 1
	v_add3_u32 v0, v27, v0, s97
	ds_write_b16_d16_hi v116, v0 offset:41072
	v_lshl_add_u64 v[40:41], v[144:145], 0, s[6:7]
	ds_read_b128 v[20:23], v215 offset:6768
	ds_read_b128 v[24:27], v215 offset:6752
	ds_read_b128 v[28:31], v215 offset:624
	ds_read_b128 v[32:35], v215 offset:608
	ds_read_b128 v[36:39], v215 offset:2160
	s_nop 0
	ds_read_b128 v[40:43], v215 offset:2144
	s_mov_b64 s[6:7], 0x1c60
	v_lshl_add_u64 v[48:49], v[144:145], 0, s[6:7]
	s_mov_b64 s[6:7], 0x2860
	ds_read_b128 v[44:47], v215 offset:3680
	s_nop 0
	ds_read_b128 v[48:51], v215 offset:3696
	v_lshl_add_u64 v[122:123], v[144:145], 0, s[6:7]
	ds_read_b128 v[118:121], v215 offset:5216
	s_nop 0
	ds_read_b128 v[122:125], v215 offset:5232
	s_mov_b64 s[6:7], 0x800
	v_lshl_add_u64 v[178:179], v[144:145], 0, s[6:7]
	s_mov_b64 s[6:7], 0x2000
	v_lshl_add_u64 v[186:187], v[144:145], 0, s[6:7]
	s_mov_b64 s[6:7], 0x2c00
	v_lshl_add_u64 v[194:195], v[144:145], 0, s[6:7]
	s_mov_b64 s[6:7], 0x820
	s_waitcnt lgkmcnt(0)
; __device__ __forceinline__ unsigned f2bf(float f) { unsigned u = __builtin_bit_cast(unsigned, f); return (u + 0x7fffu + ((u >> 16) & 1u)) >> 16; }
; DI unsigned pk2h(float lo, float hi) { const f32x2h_t v = {lo, hi}; return __builtin_bit_cast(unsigned, __builtin_convertvector(v, bf16x2h_t)); }
; DI float silu_f(float x) { return x * __builtin_amdgcn_rcpf(1.f + __expf(-x)); }
; DI void ssd_local_unit(Frame& F, int l, int ch, int g) {
;     ...
;         for (int cc = 0; cc < 4; ++cc) {
;             const int lc = cg * 32 + cc * 8, c0 = part * 256 + g * 128 + lc;
;             float acc[8];
;             { const f32x4 b0 = *(const f32x4*)(cb + c0), b1 = *(const f32x4*)(cb + c0 + 4);
; #pragma unroll
;               for (int e = 0; e < 4; ++e) { acc[e] = b0[e]; acc[4 + e] = b1[e]; } }
; #pragma unroll
;             for (int j = 0; j < 4; ++j) { float x[8]; unpack8(raw[cc][j], x);
;                 const f32x4 w0 = *(const f32x4*)(cw + j * XC + c0), w1 = *(const f32x4*)(cw + j * XC + c0 + 4);
; #pragma unroll
;                 for (int e = 0; e < 4; ++e) { acc[e] += w0[e] * okm[j] * x[e]; acc[4 + e] += w1[e] * okm[j] * x[4 + e]; } }
; #pragma unroll
;             for (int e = 0; e < 8; ++e) acc[e] = silu_f(acc[e]);
;             v4u o; o.x = pk2h(acc[0], acc[1]); o.y = pk2h(acc[2], acc[3]); o.z = pk2h(acc[4], acc[5]); o.w = pk2h(acc[6], acc[7]);
;             *(v4u*)(xbcc + (size_t)(t0 + s) * XC + c0) = o;
;             if (part == 0) { const int r2 = lc >> 6; const float dtv = DT[r2 * 128 + s], sc = dtv * __expf(AC[r2 * 128 + 127] - AC[r2 * 128 + s]);
; #pragma unroll
;                 for (int e = 0; e < 8; ++e) { XWT[(lc + e) * LP + s] = (bf16)f2bf(acc[e] * sc); XD[(lc + e) * LP + s] = (bf16)f2bf(acc[e] * dtv); } }
;             else if (part == 1) {
; #pragma unroll
;                 for (int e = 0; e < 8; ++e) BT[(lc + e) * LP + s] = (bf16)f2bf(acc[e]); }
;         } };
;     v4u ra[4][4], rb[4][4];
;     load_part(1, ra);
;     ssd_vectors(F, l, t0, g, DT, AC, RED);
;     load_part(2, rb);
;     do_part(1, ra);
;     load_part(0, ra);
	v_pk_mul_f32 v[32:33], v[140:141], v[32:33] op_sel_hi:[0,1]
	v_pk_fma_f32 v[24:25], v[32:33], v[126:127], v[24:25]
	v_lshlrev_b32_e32 v32, 16, v8
	v_and_b32_e32 v33, 0xffff0000, v8
	s_nop 0
	v_pk_mul_f32 v[40:41], v[138:139], v[40:41] op_sel_hi:[0,1]
	v_pk_fma_f32 v[24:25], v[40:41], v[32:33], v[24:25]
	v_lshlrev_b32_e32 v32, 16, v12
	v_and_b32_e32 v33, 0xffff0000, v12
	s_nop 0
	v_pk_mul_f32 v[40:41], v[136:137], v[44:45] op_sel_hi:[0,1]
	v_pk_fma_f32 v[24:25], v[40:41], v[32:33], v[24:25]
	v_lshlrev_b32_e32 v32, 16, v16
	v_and_b32_e32 v33, 0xffff0000, v16
	s_nop 0
	v_pk_mul_f32 v[40:41], v[134:135], v[118:119] op_sel_hi:[0,1]
	v_pk_fma_f32 v[24:25], v[40:41], v[32:33], v[24:25]
	v_lshlrev_b32_e32 v8, 16, v9
	v_mul_f32_e32 v0, 0xbfb8aa3b, v24
	v_exp_f32_e32 v0, v0
	v_and_b32_e32 v9, 0xffff0000, v9
	v_add_f32_e32 v0, 1.0, v0
	v_rcp_f32_e32 v32, v0
	v_mul_f32_e32 v0, 0xbfb8aa3b, v25
	v_exp_f32_e32 v0, v0
	s_nop 0
	v_add_f32_e32 v0, 1.0, v0
	v_rcp_f32_e32 v33, v0
	s_nop 0
	v_pk_mul_f32 v[24:25], v[24:25], v[32:33]
	v_pk_mul_f32 v[32:33], v[140:141], v[34:35] op_sel_hi:[0,1]
	v_pk_fma_f32 v[4:5], v[32:33], v[4:5], v[26:27]
	v_pk_mul_f32 v[26:27], v[138:139], v[42:43] op_sel_hi:[0,1]
	v_pk_fma_f32 v[4:5], v[26:27], v[8:9], v[4:5]
	v_lshlrev_b32_e32 v8, 16, v13
	v_and_b32_e32 v9, 0xffff0000, v13
	v_pk_mul_f32 v[12:13], v[136:137], v[46:47] op_sel_hi:[0,1]
	v_pk_fma_f32 v[4:5], v[12:13], v[8:9], v[4:5]
	v_lshlrev_b32_e32 v8, 16, v17
	v_and_b32_e32 v9, 0xffff0000, v17
	v_pk_mul_f32 v[12:13], v[134:135], v[120:121] op_sel_hi:[0,1]
	v_pk_fma_f32 v[4:5], v[12:13], v[8:9], v[4:5]
	v_pk_mul_f32 v[12:13], v[140:141], v[28:29] op_sel_hi:[0,1]
	v_mul_f32_e32 v0, 0xbfb8aa3b, v4
	v_exp_f32_e32 v0, v0
	v_pk_mul_f32 v[16:17], v[138:139], v[36:37] op_sel_hi:[0,1]
	v_add_f32_e32 v0, 1.0, v0
	v_rcp_f32_e32 v8, v0
	v_mul_f32_e32 v0, 0xbfb8aa3b, v5
	v_exp_f32_e32 v0, v0
	s_nop 0
	v_add_f32_e32 v0, 1.0, v0
	v_rcp_f32_e32 v9, v0
	s_nop 0
	v_pk_mul_f32 v[8:9], v[4:5], v[8:9]
	v_lshlrev_b32_e32 v4, 16, v6
	v_and_b32_e32 v5, 0xffff0000, v6
	v_pk_fma_f32 v[4:5], v[12:13], v[4:5], v[20:21]
	v_lshlrev_b32_e32 v12, 16, v10
	v_and_b32_e32 v13, 0xffff0000, v10
	v_pk_fma_f32 v[4:5], v[16:17], v[12:13], v[4:5]
	v_lshlrev_b32_e32 v12, 16, v14
	v_and_b32_e32 v13, 0xffff0000, v14
	v_pk_mul_f32 v[16:17], v[136:137], v[48:49] op_sel_hi:[0,1]
	v_pk_fma_f32 v[4:5], v[16:17], v[12:13], v[4:5]
	v_lshlrev_b32_e32 v12, 16, v18
	v_and_b32_e32 v13, 0xffff0000, v18
	s_nop 0
	v_pk_mul_f32 v[16:17], v[134:135], v[122:123] op_sel_hi:[0,1]
	v_pk_fma_f32 v[4:5], v[16:17], v[12:13], v[4:5]
	s_nop 0
	v_mul_f32_e32 v0, 0xbfb8aa3b, v4
	v_exp_f32_e32 v0, v0
	s_nop 0
	v_add_f32_e32 v0, 1.0, v0
	v_rcp_f32_e32 v12, v0
	v_mul_f32_e32 v0, 0xbfb8aa3b, v5
	v_exp_f32_e32 v0, v0
	s_nop 0
	v_add_f32_e32 v0, 1.0, v0
	v_rcp_f32_e32 v13, v0
	s_nop 0
	v_pk_mul_f32 v[12:13], v[4:5], v[12:13]
	v_lshlrev_b32_e32 v4, 16, v7
	v_and_b32_e32 v5, 0xffff0000, v7
	v_pk_mul_f32 v[6:7], v[140:141], v[30:31] op_sel_hi:[0,1]
	v_pk_fma_f32 v[4:5], v[6:7], v[4:5], v[22:23]
	v_lshlrev_b32_e32 v6, 16, v11
	v_and_b32_e32 v7, 0xffff0000, v11
	v_pk_mul_f32 v[10:11], v[138:139], v[38:39] op_sel_hi:[0,1]
	v_pk_fma_f32 v[4:5], v[10:11], v[6:7], v[4:5]
	v_lshlrev_b32_e32 v6, 16, v15
	v_and_b32_e32 v7, 0xffff0000, v15
	v_pk_mul_f32 v[10:11], v[136:137], v[50:51] op_sel_hi:[0,1]
	v_pk_fma_f32 v[4:5], v[10:11], v[6:7], v[4:5]
	v_lshlrev_b32_e32 v6, 16, v19
	v_and_b32_e32 v7, 0xffff0000, v19
	v_pk_mul_f32 v[10:11], v[134:135], v[124:125] op_sel_hi:[0,1]
	v_pk_fma_f32 v[4:5], v[10:11], v[6:7], v[4:5]
	s_nop 0
	v_mul_f32_e32 v0, 0xbfb8aa3b, v4
	v_exp_f32_e32 v0, v0
	s_nop 0
	v_add_f32_e32 v0, 1.0, v0
	v_rcp_f32_e32 v6, v0
	v_mul_f32_e32 v0, 0xbfb8aa3b, v5
	v_exp_f32_e32 v0, v0
	s_nop 0
	v_add_f32_e32 v0, 1.0, v0
	v_rcp_f32_e32 v7, v0
	v_bfe_u32 v0, v24, 16, 1
	v_add3_u32 v0, v24, v0, s97
	v_pk_mul_f32 v[10:11], v[4:5], v[6:7]
	v_cvt_pk_bf16_f32 v4, v24, v25
	v_cvt_pk_bf16_f32 v5, v8, v9
	v_cvt_pk_bf16_f32 v6, v12, v13
	v_cvt_pk_bf16_f32 v7, v10, v11
	global_store_dwordx4 v[152:153], v[4:7], off offset:560
	s_nop 1
	v_mad_u32_u24 v4, v139, s66, v135
	ds_write_b16_d16_hi v4, v0 offset:34816
	v_bfe_u32 v0, v25, 16, 1
	v_add3_u32 v0, v25, v0, s97
	ds_write_b16_d16_hi v116, v0 offset:41616
	v_bfe_u32 v0, v8, 16, 1
	v_add3_u32 v0, v8, v0, s97
	ds_write_b16_d16_hi v116, v0 offset:41888
	v_bfe_u32 v0, v9, 16, 1
	v_add3_u32 v0, v9, v0, s97
	ds_write_b16_d16_hi v116, v0 offset:42160
	v_bfe_u32 v0, v12, 16, 1
	v_add3_u32 v0, v12, v0, s97
	ds_write_b16_d16_hi v116, v0 offset:42432
	v_bfe_u32 v0, v13, 16, 1
	v_add3_u32 v0, v13, v0, s97
	ds_write_b16_d16_hi v116, v0 offset:42704
	v_bfe_u32 v0, v10, 16, 1
	v_add3_u32 v0, v10, v0, s97
	ds_write_b16_d16_hi v116, v0 offset:42976
	v_bfe_u32 v0, v11, 16, 1
	v_add3_u32 v0, v11, v0, s97
	ds_write_b16_d16_hi v116, v0 offset:43248
	global_load_dwordx4 v[4:7], v[154:155], off offset:3120
	global_load_dwordx4 v[20:23], v[154:155], off offset:3104
	global_load_dwordx4 v[36:39], v[154:155], off offset:3088
	global_load_dwordx4 v[116:119], v[154:155], off offset:3072
	global_load_dwordx4 v[8:11], v[156:157], off offset:3120
	global_load_dwordx4 v[24:27], v[156:157], off offset:3104
	global_load_dwordx4 v[40:43], v[156:157], off offset:3088
	global_load_dwordx4 v[120:123], v[156:157], off offset:3072
	global_load_dwordx4 v[12:15], v[158:159], off offset:3120
	global_load_dwordx4 v[28:31], v[158:159], off offset:3104
	global_load_dwordx4 v[44:47], v[158:159], off offset:3088
	global_load_dwordx4 v[124:127], v[158:159], off offset:3072
	global_load_dwordx4 v[16:19], v[160:161], off offset:3120
	global_load_dwordx4 v[32:35], v[160:161], off offset:3104
	global_load_dwordx4 v[48:51], v[160:161], off offset:3088
	global_load_dwordx4 v[128:131], v[160:161], off offset:3072
	ds_read_b128 v[154:157], v215 offset:7184
	s_nop 0
	ds_read_b128 v[158:161], v215 offset:7168
	ds_read_b128 v[166:169], v215 offset:1040
	ds_read_b128 v[170:173], v215 offset:1024
	ds_read_b128 v[174:177], v215 offset:2576
	s_nop 0
	ds_read_b128 v[178:181], v215 offset:2560
	s_nop 0
	ds_read_b128 v[182:185], v215 offset:4096
	s_nop 0
	ds_read_b128 v[186:189], v215 offset:4112
	s_nop 0
	ds_read_b128 v[190:193], v215 offset:5632
	s_nop 0
	ds_read_b128 v[194:197], v215 offset:5648
	s_waitcnt lgkmcnt(0)
; DI unsigned pk2h(float lo, float hi) { const f32x2h_t v = {lo, hi}; return __builtin_bit_cast(unsigned, __builtin_convertvector(v, bf16x2h_t)); }
; DI float silu_f(float x) { return x * __builtin_amdgcn_rcpf(1.f + __expf(-x)); }
; DI void ssd_local_unit(Frame& F, int l, int ch, int g) {
;     ...
;         for (int cc = 0; cc < 4; ++cc) {
;             const int lc = cg * 32 + cc * 8, c0 = part * 256 + g * 128 + lc;
;             float acc[8];
;             { const f32x4 b0 = *(const f32x4*)(cb + c0), b1 = *(const f32x4*)(cb + c0 + 4);
; #pragma unroll
;               for (int e = 0; e < 4; ++e) { acc[e] = b0[e]; acc[4 + e] = b1[e]; } }
; #pragma unroll
;             for (int j = 0; j < 4; ++j) { float x[8]; unpack8(raw[cc][j], x);
;                 const f32x4 w0 = *(const f32x4*)(cw + j * XC + c0), w1 = *(const f32x4*)(cw + j * XC + c0 + 4);
; #pragma unroll
;                 for (int e = 0; e < 4; ++e) { acc[e] += w0[e] * okm[j] * x[e]; acc[4 + e] += w1[e] * okm[j] * x[4 + e]; } }
; #pragma unroll
;             for (int e = 0; e < 8; ++e) acc[e] = silu_f(acc[e]);
;             v4u o; o.x = pk2h(acc[0], acc[1]); o.y = pk2h(acc[2], acc[3]); o.z = pk2h(acc[4], acc[5]); o.w = pk2h(acc[6], acc[7]);
;             *(v4u*)(xbcc + (size_t)(t0 + s) * XC + c0) = o;
	v_pk_mul_f32 v[170:171], v[140:141], v[170:171] op_sel_hi:[0,1]
	v_pk_fma_f32 v[158:159], v[170:171], v[198:199], v[158:159]
	v_lshlrev_b32_e32 v170, 16, v104
	v_and_b32_e32 v171, 0xffff0000, v104
	s_nop 0
	v_pk_mul_f32 v[178:179], v[138:139], v[178:179] op_sel_hi:[0,1]
	v_pk_fma_f32 v[158:159], v[178:179], v[170:171], v[158:159]
	v_lshlrev_b32_e32 v170, 16, v108
	v_and_b32_e32 v171, 0xffff0000, v108
	s_nop 0
	v_pk_mul_f32 v[178:179], v[136:137], v[182:183] op_sel_hi:[0,1]
	v_pk_fma_f32 v[158:159], v[178:179], v[170:171], v[158:159]
	v_lshlrev_b32_e32 v170, 16, v112
	v_and_b32_e32 v171, 0xffff0000, v112
	s_nop 0
	v_pk_mul_f32 v[178:179], v[134:135], v[190:191] op_sel_hi:[0,1]
	v_pk_fma_f32 v[158:159], v[178:179], v[170:171], v[158:159]
	v_lshlrev_b32_e32 v104, 16, v105
	v_mul_f32_e32 v0, 0xbfb8aa3b, v158
	v_exp_f32_e32 v0, v0
	v_and_b32_e32 v105, 0xffff0000, v105
	v_lshlrev_b32_e32 v182, 16, v84
	v_and_b32_e32 v183, 0xffff0000, v84
	v_add_f32_e32 v0, 1.0, v0
	v_rcp_f32_e32 v170, v0
	v_mul_f32_e32 v0, 0xbfb8aa3b, v159
	v_exp_f32_e32 v0, v0
	v_lshlrev_b32_e32 v84, 16, v85
	v_and_b32_e32 v85, 0xffff0000, v85
	v_add_f32_e32 v0, 1.0, v0
	v_rcp_f32_e32 v171, v0
	s_nop 0
	v_pk_mul_f32 v[158:159], v[158:159], v[170:171]
	v_pk_mul_f32 v[170:171], v[140:141], v[172:173] op_sel_hi:[0,1]
	v_pk_fma_f32 v[100:101], v[170:171], v[100:101], v[160:161]
	v_pk_mul_f32 v[160:161], v[138:139], v[180:181] op_sel_hi:[0,1]
	v_pk_fma_f32 v[100:101], v[160:161], v[104:105], v[100:101]
	v_lshlrev_b32_e32 v104, 16, v109
	v_and_b32_e32 v105, 0xffff0000, v109
	v_pk_mul_f32 v[108:109], v[136:137], v[184:185] op_sel_hi:[0,1]
	v_pk_fma_f32 v[100:101], v[108:109], v[104:105], v[100:101]
	v_lshlrev_b32_e32 v104, 16, v113
	v_and_b32_e32 v105, 0xffff0000, v113
	v_pk_mul_f32 v[108:109], v[134:135], v[192:193] op_sel_hi:[0,1]
	v_pk_fma_f32 v[100:101], v[108:109], v[104:105], v[100:101]
	v_pk_mul_f32 v[108:109], v[140:141], v[166:167] op_sel_hi:[0,1]
	v_mul_f32_e32 v0, 0xbfb8aa3b, v100
	v_exp_f32_e32 v0, v0
	v_pk_mul_f32 v[112:113], v[138:139], v[174:175] op_sel_hi:[0,1]
	v_add_f32_e32 v0, 1.0, v0
	v_rcp_f32_e32 v104, v0
	v_mul_f32_e32 v0, 0xbfb8aa3b, v101
	v_exp_f32_e32 v0, v0
	s_nop 0
	v_add_f32_e32 v0, 1.0, v0
	v_rcp_f32_e32 v105, v0
	s_nop 0
	v_pk_mul_f32 v[104:105], v[100:101], v[104:105]
	v_lshlrev_b32_e32 v100, 16, v102
	v_and_b32_e32 v101, 0xffff0000, v102
	v_pk_fma_f32 v[100:101], v[108:109], v[100:101], v[154:155]
	v_lshlrev_b32_e32 v108, 16, v106
	v_and_b32_e32 v109, 0xffff0000, v106
	v_pk_fma_f32 v[100:101], v[112:113], v[108:109], v[100:101]
	v_lshlrev_b32_e32 v108, 16, v110
	v_and_b32_e32 v109, 0xffff0000, v110
	v_pk_mul_f32 v[112:113], v[136:137], v[186:187] op_sel_hi:[0,1]
	v_pk_fma_f32 v[100:101], v[112:113], v[108:109], v[100:101]
	v_lshlrev_b32_e32 v108, 16, v114
	v_and_b32_e32 v109, 0xffff0000, v114
	s_waitcnt vmcnt(0)
	v_pk_mul_f32 v[112:113], v[134:135], v[194:195] op_sel_hi:[0,1]
	v_pk_fma_f32 v[100:101], v[112:113], v[108:109], v[100:101]
	s_nop 0
	v_mul_f32_e32 v0, 0xbfb8aa3b, v100
	v_exp_f32_e32 v0, v0
	s_nop 0
	v_add_f32_e32 v0, 1.0, v0
	v_rcp_f32_e32 v108, v0
	v_mul_f32_e32 v0, 0xbfb8aa3b, v101
	v_exp_f32_e32 v0, v0
	s_nop 0
	v_add_f32_e32 v0, 1.0, v0
	v_rcp_f32_e32 v109, v0
	s_nop 0
	v_pk_mul_f32 v[108:109], v[100:101], v[108:109]
	v_lshlrev_b32_e32 v100, 16, v103
	v_and_b32_e32 v101, 0xffff0000, v103
	v_pk_mul_f32 v[102:103], v[140:141], v[168:169] op_sel_hi:[0,1]
	v_pk_fma_f32 v[100:101], v[102:103], v[100:101], v[156:157]
	v_lshlrev_b32_e32 v102, 16, v107
	v_and_b32_e32 v103, 0xffff0000, v107
	v_pk_mul_f32 v[106:107], v[138:139], v[176:177] op_sel_hi:[0,1]
	v_pk_fma_f32 v[100:101], v[106:107], v[102:103], v[100:101]
	v_lshlrev_b32_e32 v102, 16, v111
	v_and_b32_e32 v103, 0xffff0000, v111
	v_pk_mul_f32 v[106:107], v[136:137], v[188:189] op_sel_hi:[0,1]
	v_pk_fma_f32 v[100:101], v[106:107], v[102:103], v[100:101]
	v_lshlrev_b32_e32 v102, 16, v115
	v_and_b32_e32 v103, 0xffff0000, v115
	v_pk_mul_f32 v[106:107], v[134:135], v[196:197] op_sel_hi:[0,1]
	v_pk_fma_f32 v[100:101], v[106:107], v[102:103], v[100:101]
	s_nop 0
	v_mul_f32_e32 v0, 0xbfb8aa3b, v100
	v_exp_f32_e32 v0, v0
	s_nop 0
	v_add_f32_e32 v0, 1.0, v0
	v_rcp_f32_e32 v102, v0
	v_mul_f32_e32 v0, 0xbfb8aa3b, v101
	v_exp_f32_e32 v0, v0
	s_nop 0
	v_add_f32_e32 v0, 1.0, v0
	v_rcp_f32_e32 v103, v0
	s_nop 0
	v_pk_mul_f32 v[106:107], v[100:101], v[102:103]
	v_cvt_pk_bf16_f32 v100, v158, v159
	v_cvt_pk_bf16_f32 v101, v104, v105
	v_cvt_pk_bf16_f32 v102, v108, v109
	v_cvt_pk_bf16_f32 v103, v106, v107
	global_store_dwordx4 v[152:153], v[100:103], off offset:1024
	v_lshl_add_u64 v[158:159], v[144:145], 0, s[6:7]
	ds_read_b128 v[100:103], v215 offset:7216
	ds_read_b128 v[104:107], v215 offset:7200
	ds_read_b128 v[108:111], v215 offset:1072
	ds_read_b128 v[112:115], v215 offset:1056
	ds_read_b128 v[154:157], v215 offset:2608
	s_nop 0
	ds_read_b128 v[158:161], v215 offset:2592
	s_mov_b64 s[6:7], 0x2020
	v_lshl_add_u64 v[170:171], v[144:145], 0, s[6:7]
	s_mov_b64 s[6:7], 0x2c20
	ds_read_b128 v[166:169], v215 offset:4128
	s_nop 0
	ds_read_b128 v[170:173], v215 offset:4144
	v_lshl_add_u64 v[178:179], v[144:145], 0, s[6:7]
	ds_read_b128 v[174:177], v215 offset:5664
	s_nop 0
	ds_read_b128 v[178:181], v215 offset:5680
	s_mov_b64 s[6:7], 0x840
	s_waitcnt lgkmcnt(0)
; DI unsigned pk2h(float lo, float hi) { const f32x2h_t v = {lo, hi}; return __builtin_bit_cast(unsigned, __builtin_convertvector(v, bf16x2h_t)); }
; DI float silu_f(float x) { return x * __builtin_amdgcn_rcpf(1.f + __expf(-x)); }
; DI void ssd_local_unit(Frame& F, int l, int ch, int g) {
;     ...
;         for (int cc = 0; cc < 4; ++cc) {
;             const int lc = cg * 32 + cc * 8, c0 = part * 256 + g * 128 + lc;
;             float acc[8];
;             { const f32x4 b0 = *(const f32x4*)(cb + c0), b1 = *(const f32x4*)(cb + c0 + 4);
; #pragma unroll
;               for (int e = 0; e < 4; ++e) { acc[e] = b0[e]; acc[4 + e] = b1[e]; } }
; #pragma unroll
;             for (int j = 0; j < 4; ++j) { float x[8]; unpack8(raw[cc][j], x);
;                 const f32x4 w0 = *(const f32x4*)(cw + j * XC + c0), w1 = *(const f32x4*)(cw + j * XC + c0 + 4);
; #pragma unroll
;                 for (int e = 0; e < 4; ++e) { acc[e] += w0[e] * okm[j] * x[e]; acc[4 + e] += w1[e] * okm[j] * x[4 + e]; } }
; #pragma unroll
;             for (int e = 0; e < 8; ++e) acc[e] = silu_f(acc[e]);
;             v4u o; o.x = pk2h(acc[0], acc[1]); o.y = pk2h(acc[2], acc[3]); o.z = pk2h(acc[4], acc[5]); o.w = pk2h(acc[6], acc[7]);
;             *(v4u*)(xbcc + (size_t)(t0 + s) * XC + c0) = o;
	v_pk_mul_f32 v[112:113], v[140:141], v[112:113] op_sel_hi:[0,1]
	v_pk_fma_f32 v[104:105], v[112:113], v[182:183], v[104:105]
	v_lshlrev_b32_e32 v112, 16, v88
	v_and_b32_e32 v113, 0xffff0000, v88
	s_nop 0
	v_pk_mul_f32 v[158:159], v[138:139], v[158:159] op_sel_hi:[0,1]
	v_pk_fma_f32 v[104:105], v[158:159], v[112:113], v[104:105]
	v_lshlrev_b32_e32 v112, 16, v92
	v_and_b32_e32 v113, 0xffff0000, v92
	s_nop 0
	v_pk_mul_f32 v[158:159], v[136:137], v[166:167] op_sel_hi:[0,1]
	v_pk_fma_f32 v[104:105], v[158:159], v[112:113], v[104:105]
	v_lshlrev_b32_e32 v112, 16, v96
	v_and_b32_e32 v113, 0xffff0000, v96
	s_nop 0
	v_pk_mul_f32 v[158:159], v[134:135], v[174:175] op_sel_hi:[0,1]
	v_pk_fma_f32 v[104:105], v[158:159], v[112:113], v[104:105]
	v_lshlrev_b32_e32 v88, 16, v89
	v_mul_f32_e32 v0, 0xbfb8aa3b, v104
	v_exp_f32_e32 v0, v0
	v_and_b32_e32 v89, 0xffff0000, v89
	v_lshlrev_b32_e32 v166, 16, v68
	v_and_b32_e32 v167, 0xffff0000, v68
	v_add_f32_e32 v0, 1.0, v0
	v_rcp_f32_e32 v112, v0
	v_mul_f32_e32 v0, 0xbfb8aa3b, v105
	v_exp_f32_e32 v0, v0
	v_lshlrev_b32_e32 v68, 16, v69
	v_and_b32_e32 v69, 0xffff0000, v69
	v_add_f32_e32 v0, 1.0, v0
	v_rcp_f32_e32 v113, v0
	s_nop 0
	v_pk_mul_f32 v[104:105], v[104:105], v[112:113]
	v_pk_mul_f32 v[112:113], v[140:141], v[114:115] op_sel_hi:[0,1]
	v_pk_fma_f32 v[84:85], v[112:113], v[84:85], v[106:107]
	v_pk_mul_f32 v[106:107], v[138:139], v[160:161] op_sel_hi:[0,1]
	v_pk_fma_f32 v[84:85], v[106:107], v[88:89], v[84:85]
	v_lshlrev_b32_e32 v88, 16, v93
	v_and_b32_e32 v89, 0xffff0000, v93
	v_pk_mul_f32 v[92:93], v[136:137], v[168:169] op_sel_hi:[0,1]
	v_pk_fma_f32 v[84:85], v[92:93], v[88:89], v[84:85]
	v_lshlrev_b32_e32 v88, 16, v97
	v_and_b32_e32 v89, 0xffff0000, v97
	v_pk_mul_f32 v[92:93], v[134:135], v[176:177] op_sel_hi:[0,1]
	v_pk_fma_f32 v[84:85], v[92:93], v[88:89], v[84:85]
	v_pk_mul_f32 v[92:93], v[140:141], v[108:109] op_sel_hi:[0,1]
	v_mul_f32_e32 v0, 0xbfb8aa3b, v84
	v_exp_f32_e32 v0, v0
	v_pk_mul_f32 v[96:97], v[138:139], v[154:155] op_sel_hi:[0,1]
	v_add_f32_e32 v0, 1.0, v0
	v_rcp_f32_e32 v88, v0
	v_mul_f32_e32 v0, 0xbfb8aa3b, v85
	v_exp_f32_e32 v0, v0
	s_nop 0
	v_add_f32_e32 v0, 1.0, v0
	v_rcp_f32_e32 v89, v0
	s_nop 0
	v_pk_mul_f32 v[88:89], v[84:85], v[88:89]
	v_lshlrev_b32_e32 v84, 16, v86
	v_and_b32_e32 v85, 0xffff0000, v86
	v_pk_fma_f32 v[84:85], v[92:93], v[84:85], v[100:101]
	v_lshlrev_b32_e32 v92, 16, v90
	v_and_b32_e32 v93, 0xffff0000, v90
	v_pk_fma_f32 v[84:85], v[96:97], v[92:93], v[84:85]
	v_lshlrev_b32_e32 v92, 16, v94
	v_and_b32_e32 v93, 0xffff0000, v94
	v_pk_mul_f32 v[96:97], v[136:137], v[170:171] op_sel_hi:[0,1]
	v_pk_fma_f32 v[84:85], v[96:97], v[92:93], v[84:85]
	v_lshlrev_b32_e32 v92, 16, v98
	v_and_b32_e32 v93, 0xffff0000, v98
	s_nop 0
	v_pk_mul_f32 v[96:97], v[134:135], v[178:179] op_sel_hi:[0,1]
	v_pk_fma_f32 v[84:85], v[96:97], v[92:93], v[84:85]
	s_nop 0
	v_mul_f32_e32 v0, 0xbfb8aa3b, v84
	v_exp_f32_e32 v0, v0
	s_nop 0
	v_add_f32_e32 v0, 1.0, v0
	v_rcp_f32_e32 v92, v0
	v_mul_f32_e32 v0, 0xbfb8aa3b, v85
	v_exp_f32_e32 v0, v0
	s_nop 0
	v_add_f32_e32 v0, 1.0, v0
	v_rcp_f32_e32 v93, v0
	s_nop 0
	v_pk_mul_f32 v[92:93], v[84:85], v[92:93]
	v_lshlrev_b32_e32 v84, 16, v87
	v_and_b32_e32 v85, 0xffff0000, v87
	v_pk_mul_f32 v[86:87], v[140:141], v[110:111] op_sel_hi:[0,1]
	v_pk_fma_f32 v[84:85], v[86:87], v[84:85], v[102:103]
	v_lshlrev_b32_e32 v86, 16, v91
	v_and_b32_e32 v87, 0xffff0000, v91
	v_pk_mul_f32 v[90:91], v[138:139], v[156:157] op_sel_hi:[0,1]
	v_pk_fma_f32 v[84:85], v[90:91], v[86:87], v[84:85]
	v_lshlrev_b32_e32 v86, 16, v95
	v_and_b32_e32 v87, 0xffff0000, v95
	v_pk_mul_f32 v[90:91], v[136:137], v[172:173] op_sel_hi:[0,1]
	v_pk_fma_f32 v[84:85], v[90:91], v[86:87], v[84:85]
	v_lshlrev_b32_e32 v86, 16, v99
	v_and_b32_e32 v87, 0xffff0000, v99
	v_pk_mul_f32 v[90:91], v[134:135], v[180:181] op_sel_hi:[0,1]
	v_pk_fma_f32 v[84:85], v[90:91], v[86:87], v[84:85]
	s_nop 0
	v_mul_f32_e32 v0, 0xbfb8aa3b, v84
	v_exp_f32_e32 v0, v0
	s_nop 0
	v_add_f32_e32 v0, 1.0, v0
	v_rcp_f32_e32 v86, v0
	v_mul_f32_e32 v0, 0xbfb8aa3b, v85
	v_exp_f32_e32 v0, v0
	s_nop 0
	v_add_f32_e32 v0, 1.0, v0
	v_rcp_f32_e32 v87, v0
	s_nop 0
	v_pk_mul_f32 v[90:91], v[84:85], v[86:87]
	v_cvt_pk_bf16_f32 v84, v104, v105
	v_cvt_pk_bf16_f32 v85, v88, v89
	v_cvt_pk_bf16_f32 v86, v92, v93
	v_cvt_pk_bf16_f32 v87, v90, v91
	global_store_dwordx4 v[152:153], v[84:87], off offset:1040
	v_lshl_add_u64 v[104:105], v[144:145], 0, s[6:7]
	ds_read_b128 v[84:87], v215 offset:7248
	ds_read_b128 v[88:91], v215 offset:7232
	ds_read_b128 v[92:95], v215 offset:1104
	ds_read_b128 v[96:99], v215 offset:1088
	ds_read_b128 v[100:103], v215 offset:2640
	s_nop 0
	ds_read_b128 v[104:107], v215 offset:2624
	s_mov_b64 s[6:7], 0x2040
	v_lshl_add_u64 v[112:113], v[144:145], 0, s[6:7]
	s_mov_b64 s[6:7], 0x2c40
	ds_read_b128 v[108:111], v215 offset:4160
	s_nop 0
	ds_read_b128 v[112:115], v215 offset:4176
	v_lshl_add_u64 v[158:159], v[144:145], 0, s[6:7]
	ds_read_b128 v[154:157], v215 offset:5696
	s_nop 0
	ds_read_b128 v[158:161], v215 offset:5712
	s_mov_b64 s[6:7], 0x860
	s_waitcnt lgkmcnt(0)
; DI unsigned pk2h(float lo, float hi) { const f32x2h_t v = {lo, hi}; return __builtin_bit_cast(unsigned, __builtin_convertvector(v, bf16x2h_t)); }
; DI float silu_f(float x) { return x * __builtin_amdgcn_rcpf(1.f + __expf(-x)); }
; DI void ssd_local_unit(Frame& F, int l, int ch, int g) {
;     ...
;         for (int cc = 0; cc < 4; ++cc) {
;             const int lc = cg * 32 + cc * 8, c0 = part * 256 + g * 128 + lc;
;             float acc[8];
;             { const f32x4 b0 = *(const f32x4*)(cb + c0), b1 = *(const f32x4*)(cb + c0 + 4);
; #pragma unroll
;               for (int e = 0; e < 4; ++e) { acc[e] = b0[e]; acc[4 + e] = b1[e]; } }
; #pragma unroll
;             for (int j = 0; j < 4; ++j) { float x[8]; unpack8(raw[cc][j], x);
;                 const f32x4 w0 = *(const f32x4*)(cw + j * XC + c0), w1 = *(const f32x4*)(cw + j * XC + c0 + 4);
; #pragma unroll
;                 for (int e = 0; e < 4; ++e) { acc[e] += w0[e] * okm[j] * x[e]; acc[4 + e] += w1[e] * okm[j] * x[4 + e]; } }
; #pragma unroll
;             for (int e = 0; e < 8; ++e) acc[e] = silu_f(acc[e]);
;             v4u o; o.x = pk2h(acc[0], acc[1]); o.y = pk2h(acc[2], acc[3]); o.z = pk2h(acc[4], acc[5]); o.w = pk2h(acc[6], acc[7]);
;             *(v4u*)(xbcc + (size_t)(t0 + s) * XC + c0) = o;
	v_pk_mul_f32 v[96:97], v[140:141], v[96:97] op_sel_hi:[0,1]
	v_pk_fma_f32 v[88:89], v[96:97], v[166:167], v[88:89]
	v_lshlrev_b32_e32 v96, 16, v72
	v_and_b32_e32 v97, 0xffff0000, v72
	s_nop 0
	v_pk_mul_f32 v[104:105], v[138:139], v[104:105] op_sel_hi:[0,1]
	v_pk_fma_f32 v[88:89], v[104:105], v[96:97], v[88:89]
	v_lshlrev_b32_e32 v96, 16, v76
	v_and_b32_e32 v97, 0xffff0000, v76
	s_nop 0
	v_pk_mul_f32 v[104:105], v[136:137], v[108:109] op_sel_hi:[0,1]
	v_pk_fma_f32 v[88:89], v[104:105], v[96:97], v[88:89]
	v_lshlrev_b32_e32 v96, 16, v80
	v_and_b32_e32 v97, 0xffff0000, v80
	s_nop 0
	v_pk_mul_f32 v[104:105], v[134:135], v[154:155] op_sel_hi:[0,1]
	v_pk_fma_f32 v[88:89], v[104:105], v[96:97], v[88:89]
	v_lshlrev_b32_e32 v72, 16, v73
	v_mul_f32_e32 v0, 0xbfb8aa3b, v88
	v_exp_f32_e32 v0, v0
	v_and_b32_e32 v73, 0xffff0000, v73
	v_lshlrev_b32_e32 v108, 16, v52
	v_and_b32_e32 v109, 0xffff0000, v52
	v_add_f32_e32 v0, 1.0, v0
	v_rcp_f32_e32 v96, v0
	v_mul_f32_e32 v0, 0xbfb8aa3b, v89
	v_exp_f32_e32 v0, v0
	v_lshlrev_b32_e32 v52, 16, v53
	v_and_b32_e32 v53, 0xffff0000, v53
	v_add_f32_e32 v0, 1.0, v0
	v_rcp_f32_e32 v97, v0
	s_nop 0
	v_pk_mul_f32 v[88:89], v[88:89], v[96:97]
	v_pk_mul_f32 v[96:97], v[140:141], v[98:99] op_sel_hi:[0,1]
	v_pk_fma_f32 v[68:69], v[96:97], v[68:69], v[90:91]
	v_pk_mul_f32 v[90:91], v[138:139], v[106:107] op_sel_hi:[0,1]
	v_pk_fma_f32 v[68:69], v[90:91], v[72:73], v[68:69]
	v_lshlrev_b32_e32 v72, 16, v77
	v_and_b32_e32 v73, 0xffff0000, v77
	v_pk_mul_f32 v[76:77], v[136:137], v[110:111] op_sel_hi:[0,1]
	v_pk_fma_f32 v[68:69], v[76:77], v[72:73], v[68:69]
	v_lshlrev_b32_e32 v72, 16, v81
	v_and_b32_e32 v73, 0xffff0000, v81
	v_pk_mul_f32 v[76:77], v[134:135], v[156:157] op_sel_hi:[0,1]
	v_pk_fma_f32 v[68:69], v[76:77], v[72:73], v[68:69]
	v_pk_mul_f32 v[76:77], v[140:141], v[92:93] op_sel_hi:[0,1]
	v_mul_f32_e32 v0, 0xbfb8aa3b, v68
	v_exp_f32_e32 v0, v0
	v_pk_mul_f32 v[80:81], v[138:139], v[100:101] op_sel_hi:[0,1]
	v_add_f32_e32 v0, 1.0, v0
	v_rcp_f32_e32 v72, v0
	v_mul_f32_e32 v0, 0xbfb8aa3b, v69
	v_exp_f32_e32 v0, v0
	s_nop 0
	v_add_f32_e32 v0, 1.0, v0
	v_rcp_f32_e32 v73, v0
	s_nop 0
	v_pk_mul_f32 v[72:73], v[68:69], v[72:73]
	v_lshlrev_b32_e32 v68, 16, v70
	v_and_b32_e32 v69, 0xffff0000, v70
	v_pk_fma_f32 v[68:69], v[76:77], v[68:69], v[84:85]
	v_lshlrev_b32_e32 v76, 16, v74
	v_and_b32_e32 v77, 0xffff0000, v74
	v_pk_fma_f32 v[68:69], v[80:81], v[76:77], v[68:69]
	v_lshlrev_b32_e32 v76, 16, v78
	v_and_b32_e32 v77, 0xffff0000, v78
	v_pk_mul_f32 v[80:81], v[136:137], v[112:113] op_sel_hi:[0,1]
	v_pk_fma_f32 v[68:69], v[80:81], v[76:77], v[68:69]
	v_lshlrev_b32_e32 v76, 16, v82
	v_and_b32_e32 v77, 0xffff0000, v82
	s_nop 0
	v_pk_mul_f32 v[80:81], v[134:135], v[158:159] op_sel_hi:[0,1]
	v_pk_fma_f32 v[68:69], v[80:81], v[76:77], v[68:69]
	s_nop 0
	v_mul_f32_e32 v0, 0xbfb8aa3b, v68
	v_exp_f32_e32 v0, v0
	s_nop 0
	v_add_f32_e32 v0, 1.0, v0
	v_rcp_f32_e32 v76, v0
	v_mul_f32_e32 v0, 0xbfb8aa3b, v69
	v_exp_f32_e32 v0, v0
	s_nop 0
	v_add_f32_e32 v0, 1.0, v0
	v_rcp_f32_e32 v77, v0
	s_nop 0
	v_pk_mul_f32 v[76:77], v[68:69], v[76:77]
	v_lshlrev_b32_e32 v68, 16, v71
	v_and_b32_e32 v69, 0xffff0000, v71
	v_pk_mul_f32 v[70:71], v[140:141], v[94:95] op_sel_hi:[0,1]
	v_pk_fma_f32 v[68:69], v[70:71], v[68:69], v[86:87]
	v_lshlrev_b32_e32 v70, 16, v75
	v_and_b32_e32 v71, 0xffff0000, v75
	v_pk_mul_f32 v[74:75], v[138:139], v[102:103] op_sel_hi:[0,1]
	v_pk_fma_f32 v[68:69], v[74:75], v[70:71], v[68:69]
	v_lshlrev_b32_e32 v70, 16, v79
	v_and_b32_e32 v71, 0xffff0000, v79
	v_pk_mul_f32 v[74:75], v[136:137], v[114:115] op_sel_hi:[0,1]
	v_pk_fma_f32 v[68:69], v[74:75], v[70:71], v[68:69]
	v_lshlrev_b32_e32 v70, 16, v83
	v_and_b32_e32 v71, 0xffff0000, v83
	v_pk_mul_f32 v[74:75], v[134:135], v[160:161] op_sel_hi:[0,1]
	v_pk_fma_f32 v[68:69], v[74:75], v[70:71], v[68:69]
	s_nop 0
	v_mul_f32_e32 v0, 0xbfb8aa3b, v68
	v_exp_f32_e32 v0, v0
	s_nop 0
	v_add_f32_e32 v0, 1.0, v0
	v_rcp_f32_e32 v70, v0
	v_mul_f32_e32 v0, 0xbfb8aa3b, v69
	v_exp_f32_e32 v0, v0
	s_nop 0
	v_add_f32_e32 v0, 1.0, v0
	v_rcp_f32_e32 v71, v0
	s_nop 0
	v_pk_mul_f32 v[74:75], v[68:69], v[70:71]
	v_cvt_pk_bf16_f32 v68, v88, v89
	v_cvt_pk_bf16_f32 v69, v72, v73
	v_cvt_pk_bf16_f32 v70, v76, v77
	v_cvt_pk_bf16_f32 v71, v74, v75
	global_store_dwordx4 v[152:153], v[68:71], off offset:1056
	v_lshl_add_u64 v[88:89], v[144:145], 0, s[6:7]
	ds_read_b128 v[68:71], v215 offset:7280
	ds_read_b128 v[72:75], v215 offset:7264
	ds_read_b128 v[76:79], v215 offset:1136
	ds_read_b128 v[80:83], v215 offset:1120
	ds_read_b128 v[84:87], v215 offset:2672
	s_nop 0
	ds_read_b128 v[88:91], v215 offset:2656
	s_mov_b64 s[6:7], 0x2060
	v_lshl_add_u64 v[96:97], v[144:145], 0, s[6:7]
	s_mov_b64 s[6:7], 0x2c60
	ds_read_b128 v[92:95], v215 offset:4192
	s_nop 0
	ds_read_b128 v[96:99], v215 offset:4208
	v_lshl_add_u64 v[104:105], v[144:145], 0, s[6:7]
	ds_read_b128 v[100:103], v215 offset:5728
	s_nop 0
	ds_read_b128 v[104:107], v215 offset:5744
	s_mov_b64 s[6:7], 0x1800
	s_waitcnt lgkmcnt(0)
; DI unsigned pk2h(float lo, float hi) { const f32x2h_t v = {lo, hi}; return __builtin_bit_cast(unsigned, __builtin_convertvector(v, bf16x2h_t)); }
; DI float silu_f(float x) { return x * __builtin_amdgcn_rcpf(1.f + __expf(-x)); }
; DI void ssd_local_unit(Frame& F, int l, int ch, int g) {
;     ...
;         for (int cc = 0; cc < 4; ++cc) {
;             const int lc = cg * 32 + cc * 8, c0 = part * 256 + g * 128 + lc;
;             float acc[8];
;             { const f32x4 b0 = *(const f32x4*)(cb + c0), b1 = *(const f32x4*)(cb + c0 + 4);
; #pragma unroll
;               for (int e = 0; e < 4; ++e) { acc[e] = b0[e]; acc[4 + e] = b1[e]; } }
; #pragma unroll
;             for (int j = 0; j < 4; ++j) { float x[8]; unpack8(raw[cc][j], x);
;                 const f32x4 w0 = *(const f32x4*)(cw + j * XC + c0), w1 = *(const f32x4*)(cw + j * XC + c0 + 4);
; #pragma unroll
;                 for (int e = 0; e < 4; ++e) { acc[e] += w0[e] * okm[j] * x[e]; acc[4 + e] += w1[e] * okm[j] * x[4 + e]; } }
; #pragma unroll
;             for (int e = 0; e < 8; ++e) acc[e] = silu_f(acc[e]);
;             v4u o; o.x = pk2h(acc[0], acc[1]); o.y = pk2h(acc[2], acc[3]); o.z = pk2h(acc[4], acc[5]); o.w = pk2h(acc[6], acc[7]);
;             *(v4u*)(xbcc + (size_t)(t0 + s) * XC + c0) = o;
	v_pk_mul_f32 v[80:81], v[140:141], v[80:81] op_sel_hi:[0,1]
	v_pk_fma_f32 v[72:73], v[80:81], v[108:109], v[72:73]
	v_lshlrev_b32_e32 v80, 16, v56
	v_and_b32_e32 v81, 0xffff0000, v56
	s_nop 0
	v_pk_mul_f32 v[88:89], v[138:139], v[88:89] op_sel_hi:[0,1]
	v_pk_fma_f32 v[72:73], v[88:89], v[80:81], v[72:73]
	v_lshlrev_b32_e32 v80, 16, v60
	v_and_b32_e32 v81, 0xffff0000, v60
	s_nop 0
	v_pk_mul_f32 v[88:89], v[136:137], v[92:93] op_sel_hi:[0,1]
	v_pk_fma_f32 v[72:73], v[88:89], v[80:81], v[72:73]
	v_lshlrev_b32_e32 v80, 16, v64
	v_and_b32_e32 v81, 0xffff0000, v64
	s_nop 0
	v_pk_mul_f32 v[88:89], v[134:135], v[100:101] op_sel_hi:[0,1]
	v_pk_fma_f32 v[72:73], v[88:89], v[80:81], v[72:73]
	v_lshlrev_b32_e32 v56, 16, v57
	v_mul_f32_e32 v0, 0xbfb8aa3b, v72
	v_exp_f32_e32 v0, v0
	v_and_b32_e32 v57, 0xffff0000, v57
	v_lshlrev_b32_e32 v92, 16, v116
	v_and_b32_e32 v93, 0xffff0000, v116
	v_add_f32_e32 v0, 1.0, v0
	v_rcp_f32_e32 v80, v0
	v_mul_f32_e32 v0, 0xbfb8aa3b, v73
	v_exp_f32_e32 v0, v0
	s_nop 0
	v_add_f32_e32 v0, 1.0, v0
	v_rcp_f32_e32 v81, v0
	s_nop 0
	v_pk_mul_f32 v[72:73], v[72:73], v[80:81]
	v_pk_mul_f32 v[80:81], v[140:141], v[82:83] op_sel_hi:[0,1]
	v_pk_fma_f32 v[52:53], v[80:81], v[52:53], v[74:75]
	v_pk_mul_f32 v[74:75], v[138:139], v[90:91] op_sel_hi:[0,1]
	v_pk_fma_f32 v[52:53], v[74:75], v[56:57], v[52:53]
	v_lshlrev_b32_e32 v56, 16, v61
	v_and_b32_e32 v57, 0xffff0000, v61
	v_pk_mul_f32 v[60:61], v[136:137], v[94:95] op_sel_hi:[0,1]
	v_pk_fma_f32 v[52:53], v[60:61], v[56:57], v[52:53]
	v_lshlrev_b32_e32 v56, 16, v65
	v_and_b32_e32 v57, 0xffff0000, v65
	v_pk_mul_f32 v[60:61], v[134:135], v[102:103] op_sel_hi:[0,1]
	v_pk_fma_f32 v[52:53], v[60:61], v[56:57], v[52:53]
	v_pk_mul_f32 v[60:61], v[140:141], v[76:77] op_sel_hi:[0,1]
	v_mul_f32_e32 v0, 0xbfb8aa3b, v52
	v_exp_f32_e32 v0, v0
	v_pk_mul_f32 v[64:65], v[138:139], v[84:85] op_sel_hi:[0,1]
	v_lshl_add_u64 v[80:81], v[144:145], 0, s[6:7]
	s_mov_b64 s[6:7], 0x2400
	v_add_f32_e32 v0, 1.0, v0
	v_rcp_f32_e32 v56, v0
	v_mul_f32_e32 v0, 0xbfb8aa3b, v53
	v_exp_f32_e32 v0, v0
	v_lshl_add_u64 v[88:89], v[144:145], 0, s[6:7]
	s_movk_i32 s6, 0x2000
	v_add_f32_e32 v0, 1.0, v0
	v_rcp_f32_e32 v57, v0
	s_nop 0
	v_pk_mul_f32 v[56:57], v[52:53], v[56:57]
	v_lshlrev_b32_e32 v52, 16, v54
	v_and_b32_e32 v53, 0xffff0000, v54
	v_pk_fma_f32 v[52:53], v[60:61], v[52:53], v[68:69]
	v_lshlrev_b32_e32 v60, 16, v58
	v_and_b32_e32 v61, 0xffff0000, v58
	v_pk_fma_f32 v[52:53], v[64:65], v[60:61], v[52:53]
	v_lshlrev_b32_e32 v60, 16, v62
	v_and_b32_e32 v61, 0xffff0000, v62
	v_pk_mul_f32 v[64:65], v[136:137], v[96:97] op_sel_hi:[0,1]
	v_pk_fma_f32 v[52:53], v[64:65], v[60:61], v[52:53]
	v_lshlrev_b32_e32 v60, 16, v66
	v_and_b32_e32 v61, 0xffff0000, v66
	s_nop 0
	v_pk_mul_f32 v[64:65], v[134:135], v[104:105] op_sel_hi:[0,1]
	v_pk_fma_f32 v[52:53], v[64:65], v[60:61], v[52:53]
	s_nop 0
	v_mul_f32_e32 v0, 0xbfb8aa3b, v52
	v_exp_f32_e32 v0, v0
	s_nop 0
	v_add_f32_e32 v0, 1.0, v0
	v_rcp_f32_e32 v60, v0
	v_mul_f32_e32 v0, 0xbfb8aa3b, v53
	v_exp_f32_e32 v0, v0
	s_nop 0
	v_add_f32_e32 v0, 1.0, v0
	v_rcp_f32_e32 v61, v0
	s_nop 0
	v_pk_mul_f32 v[60:61], v[52:53], v[60:61]
	v_lshlrev_b32_e32 v52, 16, v55
	v_and_b32_e32 v53, 0xffff0000, v55
	v_pk_mul_f32 v[54:55], v[140:141], v[78:79] op_sel_hi:[0,1]
	v_pk_fma_f32 v[52:53], v[54:55], v[52:53], v[70:71]
	v_lshlrev_b32_e32 v54, 16, v59
	v_and_b32_e32 v55, 0xffff0000, v59
	v_pk_mul_f32 v[58:59], v[138:139], v[86:87] op_sel_hi:[0,1]
	v_pk_fma_f32 v[52:53], v[58:59], v[54:55], v[52:53]
	v_lshlrev_b32_e32 v54, 16, v63
	v_and_b32_e32 v55, 0xffff0000, v63
	v_pk_mul_f32 v[58:59], v[136:137], v[98:99] op_sel_hi:[0,1]
	v_pk_fma_f32 v[52:53], v[58:59], v[54:55], v[52:53]
	v_lshlrev_b32_e32 v54, 16, v67
	v_and_b32_e32 v55, 0xffff0000, v67
	v_pk_mul_f32 v[58:59], v[134:135], v[106:107] op_sel_hi:[0,1]
	v_pk_fma_f32 v[52:53], v[58:59], v[54:55], v[52:53]
	v_lshlrev_b32_e32 v106, 16, v36
	v_mul_f32_e32 v0, 0xbfb8aa3b, v52
	v_exp_f32_e32 v0, v0
	v_and_b32_e32 v107, 0xffff0000, v36
	v_lshlrev_b32_e32 v36, 16, v37
	v_and_b32_e32 v37, 0xffff0000, v37
	v_add_f32_e32 v0, 1.0, v0
	v_rcp_f32_e32 v54, v0
	v_mul_f32_e32 v0, 0xbfb8aa3b, v53
	v_exp_f32_e32 v0, v0
	s_nop 0
	v_add_f32_e32 v0, 1.0, v0
	v_rcp_f32_e32 v55, v0
	s_nop 0
	v_pk_mul_f32 v[58:59], v[52:53], v[54:55]
	v_cvt_pk_bf16_f32 v52, v72, v73
	v_cvt_pk_bf16_f32 v53, v56, v57
	v_cvt_pk_bf16_f32 v54, v60, v61
	v_cvt_pk_bf16_f32 v55, v58, v59
	global_store_dwordx4 v[152:153], v[52:55], off offset:1072
	ds_read_b128 v[56:59], v215 offset:6160
	s_nop 0
	ds_read_b128 v[52:55], v215 offset:6144
	ds_read_b128 v[60:63], v215 offset:16
	ds_read_b128 v[64:67], v215 offset:0
	ds_read_b128 v[68:71], v215 offset:1552
	ds_read_b128 v[72:75], v215 offset:1536
	ds_read_b128 v[76:79], v215 offset:3072
	s_nop 0
	ds_read_b128 v[80:83], v215 offset:3088
	s_nop 0
	ds_read_b128 v[84:87], v215 offset:4608
	s_nop 0
	ds_read_b128 v[88:91], v215 offset:4624
	s_waitcnt lgkmcnt(0)
; DI unsigned pk2h(float lo, float hi) { const f32x2h_t v = {lo, hi}; return __builtin_bit_cast(unsigned, __builtin_convertvector(v, bf16x2h_t)); }
; DI float silu_f(float x) { return x * __builtin_amdgcn_rcpf(1.f + __expf(-x)); }
; DI void ssd_local_unit(Frame& F, int l, int ch, int g) {
;     ...
;         for (int cc = 0; cc < 4; ++cc) {
;             const int lc = cg * 32 + cc * 8, c0 = part * 256 + g * 128 + lc;
;             float acc[8];
;             { const f32x4 b0 = *(const f32x4*)(cb + c0), b1 = *(const f32x4*)(cb + c0 + 4);
; #pragma unroll
;               for (int e = 0; e < 4; ++e) { acc[e] = b0[e]; acc[4 + e] = b1[e]; } }
; #pragma unroll
;             for (int j = 0; j < 4; ++j) { float x[8]; unpack8(raw[cc][j], x);
;                 const f32x4 w0 = *(const f32x4*)(cw + j * XC + c0), w1 = *(const f32x4*)(cw + j * XC + c0 + 4);
; #pragma unroll
;                 for (int e = 0; e < 4; ++e) { acc[e] += w0[e] * okm[j] * x[e]; acc[4 + e] += w1[e] * okm[j] * x[4 + e]; } }
; #pragma unroll
;             for (int e = 0; e < 8; ++e) acc[e] = silu_f(acc[e]);
;             v4u o; o.x = pk2h(acc[0], acc[1]); o.y = pk2h(acc[2], acc[3]); o.z = pk2h(acc[4], acc[5]); o.w = pk2h(acc[6], acc[7]);
;             *(v4u*)(xbcc + (size_t)(t0 + s) * XC + c0) = o;
;             if (part == 0) { const int r2 = lc >> 6; const float dtv = DT[r2 * 128 + s], sc = dtv * __expf(AC[r2 * 128 + 127] - AC[r2 * 128 + s]);
	v_pk_mul_f32 v[60:61], v[140:141], v[60:61] op_sel_hi:[0,1]
	s_nop 0
	v_pk_mul_f32 v[64:65], v[140:141], v[64:65] op_sel_hi:[0,1]
	v_pk_fma_f32 v[52:53], v[64:65], v[92:93], v[52:53]
	v_lshlrev_b32_e32 v64, 16, v120
	v_and_b32_e32 v65, 0xffff0000, v120
	s_nop 0
	v_pk_mul_f32 v[72:73], v[138:139], v[72:73] op_sel_hi:[0,1]
	v_pk_fma_f32 v[52:53], v[72:73], v[64:65], v[52:53]
	v_lshlrev_b32_e32 v64, 16, v124
	v_and_b32_e32 v65, 0xffff0000, v124
	s_nop 0
	v_pk_mul_f32 v[72:73], v[136:137], v[76:77] op_sel_hi:[0,1]
	v_pk_fma_f32 v[52:53], v[72:73], v[64:65], v[52:53]
	v_lshlrev_b32_e32 v64, 16, v128
	v_and_b32_e32 v65, 0xffff0000, v128
	s_nop 0
	v_pk_mul_f32 v[72:73], v[134:135], v[84:85] op_sel_hi:[0,1]
	v_pk_fma_f32 v[52:53], v[72:73], v[64:65], v[52:53]
	v_pk_mul_f32 v[66:67], v[140:141], v[66:67] op_sel_hi:[0,1]
	v_mul_f32_e32 v0, 0xbfb8aa3b, v52
	v_exp_f32_e32 v0, v0
	v_pk_mul_f32 v[62:63], v[140:141], v[62:63] op_sel_hi:[0,1]
	v_add_f32_e32 v0, 1.0, v0
	v_rcp_f32_e32 v64, v0
	v_mul_f32_e32 v0, 0xbfb8aa3b, v53
	v_exp_f32_e32 v0, v0
	s_nop 0
	v_add_f32_e32 v0, 1.0, v0
	v_rcp_f32_e32 v65, v0
	s_nop 0
	v_pk_mul_f32 v[52:53], v[52:53], v[64:65]
	v_lshlrev_b32_e32 v64, 16, v117
	v_and_b32_e32 v65, 0xffff0000, v117
	v_pk_fma_f32 v[54:55], v[66:67], v[64:65], v[54:55]
	v_lshlrev_b32_e32 v64, 16, v121
	v_and_b32_e32 v65, 0xffff0000, v121
	v_pk_mul_f32 v[66:67], v[138:139], v[74:75] op_sel_hi:[0,1]
	v_pk_fma_f32 v[54:55], v[66:67], v[64:65], v[54:55]
	v_lshlrev_b32_e32 v64, 16, v125
	v_and_b32_e32 v65, 0xffff0000, v125
	v_pk_mul_f32 v[66:67], v[136:137], v[78:79] op_sel_hi:[0,1]
	v_pk_fma_f32 v[54:55], v[66:67], v[64:65], v[54:55]
	v_lshlrev_b32_e32 v64, 16, v129
	v_and_b32_e32 v65, 0xffff0000, v129
	v_pk_mul_f32 v[66:67], v[134:135], v[86:87] op_sel_hi:[0,1]
	v_pk_fma_f32 v[54:55], v[66:67], v[64:65], v[54:55]
	s_nop 0
	v_mul_f32_e32 v0, 0xbfb8aa3b, v54
	v_exp_f32_e32 v0, v0
	s_nop 0
	v_add_f32_e32 v0, 1.0, v0
	v_rcp_f32_e32 v64, v0
	v_mul_f32_e32 v0, 0xbfb8aa3b, v55
	v_exp_f32_e32 v0, v0
	s_nop 0
	v_add_f32_e32 v0, 1.0, v0
	v_rcp_f32_e32 v65, v0
	s_nop 0
	v_pk_mul_f32 v[54:55], v[54:55], v[64:65]
	v_lshlrev_b32_e32 v64, 16, v118
	v_and_b32_e32 v65, 0xffff0000, v118
	v_pk_fma_f32 v[56:57], v[60:61], v[64:65], v[56:57]
	v_lshlrev_b32_e32 v60, 16, v122
	v_and_b32_e32 v61, 0xffff0000, v122
	v_pk_mul_f32 v[64:65], v[138:139], v[68:69] op_sel_hi:[0,1]
	v_pk_fma_f32 v[56:57], v[64:65], v[60:61], v[56:57]
	v_lshlrev_b32_e32 v60, 16, v126
	v_and_b32_e32 v61, 0xffff0000, v126
	v_pk_mul_f32 v[64:65], v[136:137], v[80:81] op_sel_hi:[0,1]
	v_pk_fma_f32 v[56:57], v[64:65], v[60:61], v[56:57]
	v_lshlrev_b32_e32 v60, 16, v130
	v_and_b32_e32 v61, 0xffff0000, v130
	s_nop 0
	v_pk_mul_f32 v[64:65], v[134:135], v[88:89] op_sel_hi:[0,1]
	v_pk_fma_f32 v[56:57], v[64:65], v[60:61], v[56:57]
	v_add_u32_e32 v64, s4, v164
	v_mul_f32_e32 v0, 0xbfb8aa3b, v56
	v_exp_f32_e32 v0, v0
	s_nop 0
	v_add_f32_e32 v0, 1.0, v0
	v_rcp_f32_e32 v60, v0
	v_mul_f32_e32 v0, 0xbfb8aa3b, v57
	v_exp_f32_e32 v0, v0
	s_nop 0
	v_add_f32_e32 v0, 1.0, v0
	v_rcp_f32_e32 v61, v0
	s_nop 0
	v_pk_mul_f32 v[56:57], v[56:57], v[60:61]
	v_lshlrev_b32_e32 v60, 16, v119
	v_and_b32_e32 v61, 0xffff0000, v119
	v_pk_fma_f32 v[58:59], v[62:63], v[60:61], v[58:59]
	v_lshlrev_b32_e32 v60, 16, v123
	v_and_b32_e32 v61, 0xffff0000, v123
	v_pk_mul_f32 v[62:63], v[138:139], v[70:71] op_sel_hi:[0,1]
	v_pk_fma_f32 v[58:59], v[62:63], v[60:61], v[58:59]
	v_lshlrev_b32_e32 v60, 16, v127
	v_and_b32_e32 v61, 0xffff0000, v127
	v_pk_mul_f32 v[62:63], v[136:137], v[82:83] op_sel_hi:[0,1]
	v_pk_fma_f32 v[58:59], v[62:63], v[60:61], v[58:59]
	v_lshlrev_b32_e32 v60, 16, v131
	v_and_b32_e32 v61, 0xffff0000, v131
	v_pk_mul_f32 v[62:63], v[134:135], v[90:91] op_sel_hi:[0,1]
	v_pk_fma_f32 v[58:59], v[62:63], v[60:61], v[58:59]
	v_cvt_pk_bf16_f32 v62, v56, v57
	v_mul_f32_e32 v0, 0xbfb8aa3b, v58
	v_exp_f32_e32 v0, v0
	s_nop 0
	v_add_f32_e32 v0, 1.0, v0
	v_rcp_f32_e32 v60, v0
	v_mul_f32_e32 v0, 0xbfb8aa3b, v59
	v_exp_f32_e32 v0, v0
	s_nop 0
	v_add_f32_e32 v0, 1.0, v0
	v_rcp_f32_e32 v61, v0
	v_and_b32_e32 v0, 0x80, v2
	v_add_lshl_u32 v0, v0, v1, 2
	v_add_u32_e32 v2, s41, v0
	v_pk_mul_f32 v[58:59], v[58:59], v[60:61]
	v_cvt_pk_bf16_f32 v60, v52, v53
	v_cvt_pk_bf16_f32 v61, v54, v55
	v_cvt_pk_bf16_f32 v63, v58, v59
	v_add_u32_e32 v0, s36, v0
	global_store_dwordx4 v[152:153], v[60:63], off
	ds_read_b32 v60, v2
	ds_read_b32 v0, v0
	v_lshl_or_b32 v2, v137, 8, v233
	v_add_u32_e32 v2, s36, v2
	ds_read_b32 v2, v2
	s_waitcnt lgkmcnt(0)
; __device__ __forceinline__ unsigned f2bf(float f) { unsigned u = __builtin_bit_cast(unsigned, f); return (u + 0x7fffu + ((u >> 16) & 1u)) >> 16; }
; DI unsigned pk2h(float lo, float hi) { const f32x2h_t v = {lo, hi}; return __builtin_bit_cast(unsigned, __builtin_convertvector(v, bf16x2h_t)); }
; DI float silu_f(float x) { return x * __builtin_amdgcn_rcpf(1.f + __expf(-x)); }
; DI void ssd_local_unit(Frame& F, int l, int ch, int g) {
;     ...
;         for (int cc = 0; cc < 4; ++cc) {
;             const int lc = cg * 32 + cc * 8, c0 = part * 256 + g * 128 + lc;
;             float acc[8];
;             { const f32x4 b0 = *(const f32x4*)(cb + c0), b1 = *(const f32x4*)(cb + c0 + 4);
; #pragma unroll
;               for (int e = 0; e < 4; ++e) { acc[e] = b0[e]; acc[4 + e] = b1[e]; } }
; #pragma unroll
;             for (int j = 0; j < 4; ++j) { float x[8]; unpack8(raw[cc][j], x);
;                 const f32x4 w0 = *(const f32x4*)(cw + j * XC + c0), w1 = *(const f32x4*)(cw + j * XC + c0 + 4);
; #pragma unroll
;                 for (int e = 0; e < 4; ++e) { acc[e] += w0[e] * okm[j] * x[e]; acc[4 + e] += w1[e] * okm[j] * x[4 + e]; } }
; #pragma unroll
;             for (int e = 0; e < 8; ++e) acc[e] = silu_f(acc[e]);
;             v4u o; o.x = pk2h(acc[0], acc[1]); o.y = pk2h(acc[2], acc[3]); o.z = pk2h(acc[4], acc[5]); o.w = pk2h(acc[6], acc[7]);
;             *(v4u*)(xbcc + (size_t)(t0 + s) * XC + c0) = o;
;             if (part == 0) { const int r2 = lc >> 6; const float dtv = DT[r2 * 128 + s], sc = dtv * __expf(AC[r2 * 128 + 127] - AC[r2 * 128 + s]);
; #pragma unroll
;                 for (int e = 0; e < 8; ++e) { XWT[(lc + e) * LP + s] = (bf16)f2bf(acc[e] * sc); XD[(lc + e) * LP + s] = (bf16)f2bf(acc[e] * dtv); } }
	v_sub_f32_e32 v0, v2, v0
	v_mul_f32_e32 v0, 0x3fb8aa3b, v0
	v_exp_f32_e32 v0, v0
	s_nop 0
	v_mul_f32_e32 v61, v60, v0
	v_mul_f32_e32 v0, v61, v52
	v_bfe_u32 v2, v0, 16, 1
	v_add3_u32 v0, v0, v2, s97
	v_mul_u32_u24_e32 v2, 0x1100, v137
	v_lshlrev_b32_e32 v2, 1, v2
	v_add_u32_e32 v62, v135, v2
	ds_write_b16_d16_hi v62, v0
	v_mul_f32_e32 v0, v60, v52
	v_bfe_u32 v52, v0, 16, 1
	v_add3_u32 v0, v0, v52, s97
	v_add_u32_e32 v63, v64, v2
	ds_write_b16_d16_hi v63, v0
	v_mul_f32_e32 v0, v61, v53
	v_bfe_u32 v2, v0, 16, 1
	v_add3_u32 v0, v0, v2, s97
	ds_write_b16_d16_hi v62, v0 offset:272
	v_mul_f32_e32 v0, v60, v53
	v_bfe_u32 v2, v0, 16, 1
	v_add3_u32 v0, v0, v2, s97
	ds_write_b16_d16_hi v63, v0 offset:272
	v_mul_f32_e32 v0, v61, v54
	v_bfe_u32 v2, v0, 16, 1
	v_add3_u32 v0, v0, v2, s97
	ds_write_b16_d16_hi v62, v0 offset:544
	v_mul_f32_e32 v0, v60, v54
	v_bfe_u32 v2, v0, 16, 1
	v_add3_u32 v0, v0, v2, s97
	ds_write_b16_d16_hi v63, v0 offset:544
	v_mul_f32_e32 v0, v61, v55
	v_bfe_u32 v2, v0, 16, 1
	v_add3_u32 v0, v0, v2, s97
	ds_write_b16_d16_hi v62, v0 offset:816
	v_mul_f32_e32 v0, v60, v55
	v_bfe_u32 v2, v0, 16, 1
	v_add3_u32 v0, v0, v2, s97
	ds_write_b16_d16_hi v63, v0 offset:816
	v_mul_f32_e32 v0, v61, v56
	v_bfe_u32 v2, v0, 16, 1
	v_add3_u32 v0, v0, v2, s97
	ds_write_b16_d16_hi v62, v0 offset:1088
	v_mul_f32_e32 v0, v60, v56
	v_bfe_u32 v2, v0, 16, 1
	v_add3_u32 v0, v0, v2, s97
	ds_write_b16_d16_hi v63, v0 offset:1088
	v_mul_f32_e32 v0, v61, v57
	v_bfe_u32 v2, v0, 16, 1
	v_add3_u32 v0, v0, v2, s97
	ds_write_b16_d16_hi v62, v0 offset:1360
	v_mul_f32_e32 v0, v60, v57
	v_bfe_u32 v2, v0, 16, 1
	v_add3_u32 v0, v0, v2, s97
	ds_write_b16_d16_hi v63, v0 offset:1360
	v_mul_f32_e32 v0, v61, v58
	v_bfe_u32 v2, v0, 16, 1
	v_add3_u32 v0, v0, v2, s97
	ds_write_b16_d16_hi v62, v0 offset:1632
	v_mul_f32_e32 v0, v60, v58
	v_bfe_u32 v2, v0, 16, 1
	v_add3_u32 v0, v0, v2, s97
	ds_write_b16_d16_hi v63, v0 offset:1632
	v_mul_f32_e32 v0, v61, v59
	v_bfe_u32 v2, v0, 16, 1
	v_add3_u32 v0, v0, v2, s97
	ds_write_b16_d16_hi v62, v0 offset:1904
	v_mul_f32_e32 v0, v60, v59
	v_bfe_u32 v2, v0, 16, 1
	v_add3_u32 v0, v0, v2, s97
	v_add_u32_e32 v2, s40, v141
	v_lshlrev_b64 v[52:53], 2, v[2:3]
	v_lshl_add_u64 v[58:59], s[2:3], 0, v[52:53]
	v_lshl_add_u64 v[52:53], s[0:1], 0, v[52:53]
	ds_write_b16_d16_hi v63, v0 offset:1904
	s_mov_b64 s[0:1], 0x1820
	v_add_co_u32_e32 v54, vcc, s64, v52
	global_load_dwordx4 v[66:69], v[58:59], off offset:48
	global_load_dwordx4 v[70:73], v[58:59], off offset:32
	global_load_dwordx4 v[74:77], v[52:53], off offset:48
	global_load_dwordx4 v[78:81], v[52:53], off offset:32
	global_load_dwordx4 v[82:85], v[52:53], off offset:3120
	global_load_dwordx4 v[86:89], v[52:53], off offset:3104
	v_lshl_add_u64 v[56:57], v[52:53], 0, s[0:1]
	v_addc_co_u32_e32 v55, vcc, 0, v53, vcc
	global_load_dwordx4 v[90:93], v[54:55], off offset:2080
	global_load_dwordx4 v[94:97], v[56:57], off offset:16
	s_mov_b64 s[0:1], 0x2420
	v_add_co_u32_e32 v56, vcc, s42, v52
	v_lshl_add_u64 v[102:103], v[52:53], 0, s[0:1]
	s_nop 0
	v_addc_co_u32_e32 v57, vcc, 0, v53, vcc
	global_load_dwordx4 v[98:101], v[56:57], off offset:1056
	s_nop 0
	global_load_dwordx4 v[102:105], v[102:103], off offset:16
	s_mov_b64 s[0:1], 0x1840
	s_or_b32 s2, s39, s18
	s_waitcnt vmcnt(6)
	v_pk_mul_f32 v[78:79], v[140:141], v[78:79] op_sel_hi:[0,1]
	v_pk_fma_f32 v[70:71], v[78:79], v[106:107], v[70:71]
	v_lshlrev_b32_e32 v78, 16, v40
	v_and_b32_e32 v79, 0xffff0000, v40
	s_waitcnt vmcnt(4)
	v_pk_mul_f32 v[86:87], v[138:139], v[86:87] op_sel_hi:[0,1]
	v_pk_fma_f32 v[70:71], v[86:87], v[78:79], v[70:71]
	v_lshlrev_b32_e32 v78, 16, v44
	v_and_b32_e32 v79, 0xffff0000, v44
	s_waitcnt vmcnt(3)
	v_pk_mul_f32 v[86:87], v[136:137], v[90:91] op_sel_hi:[0,1]
	v_pk_fma_f32 v[70:71], v[86:87], v[78:79], v[70:71]
	v_lshlrev_b32_e32 v78, 16, v48
	v_and_b32_e32 v79, 0xffff0000, v48
	s_waitcnt vmcnt(1)
	v_pk_mul_f32 v[86:87], v[134:135], v[98:99] op_sel_hi:[0,1]
	v_pk_fma_f32 v[70:71], v[86:87], v[78:79], v[70:71]
	v_lshlrev_b32_e32 v40, 16, v41
	v_mul_f32_e32 v0, 0xbfb8aa3b, v70
	v_exp_f32_e32 v0, v0
	v_and_b32_e32 v41, 0xffff0000, v41
	v_add_f32_e32 v0, 1.0, v0
	v_rcp_f32_e32 v78, v0
	v_mul_f32_e32 v0, 0xbfb8aa3b, v71
	v_exp_f32_e32 v0, v0
	s_nop 0
	v_add_f32_e32 v0, 1.0, v0
	v_rcp_f32_e32 v79, v0
	s_nop 0
	v_pk_mul_f32 v[70:71], v[70:71], v[78:79]
	v_pk_mul_f32 v[78:79], v[140:141], v[80:81] op_sel_hi:[0,1]
	v_pk_fma_f32 v[36:37], v[78:79], v[36:37], v[72:73]
	v_pk_mul_f32 v[72:73], v[138:139], v[88:89] op_sel_hi:[0,1]
	v_pk_fma_f32 v[36:37], v[72:73], v[40:41], v[36:37]
	v_lshlrev_b32_e32 v40, 16, v45
	v_and_b32_e32 v41, 0xffff0000, v45
	v_pk_mul_f32 v[44:45], v[136:137], v[92:93] op_sel_hi:[0,1]
	v_pk_fma_f32 v[36:37], v[44:45], v[40:41], v[36:37]
	v_lshlrev_b32_e32 v40, 16, v49
	v_and_b32_e32 v41, 0xffff0000, v49
	v_pk_mul_f32 v[44:45], v[134:135], v[100:101] op_sel_hi:[0,1]
	v_pk_fma_f32 v[36:37], v[44:45], v[40:41], v[36:37]
	v_pk_mul_f32 v[48:49], v[138:139], v[82:83] op_sel_hi:[0,1]
	v_mul_f32_e32 v0, 0xbfb8aa3b, v36
	v_exp_f32_e32 v0, v0
	s_nop 0
	v_add_f32_e32 v0, 1.0, v0
	v_rcp_f32_e32 v40, v0
	v_mul_f32_e32 v0, 0xbfb8aa3b, v37
	v_exp_f32_e32 v0, v0
	s_nop 0
	v_add_f32_e32 v0, 1.0, v0
	v_rcp_f32_e32 v41, v0
	s_nop 0
	v_pk_mul_f32 v[44:45], v[36:37], v[40:41]
	v_lshlrev_b32_e32 v36, 16, v38
	v_and_b32_e32 v37, 0xffff0000, v38
	v_pk_mul_f32 v[40:41], v[140:141], v[74:75] op_sel_hi:[0,1]
	v_pk_fma_f32 v[36:37], v[40:41], v[36:37], v[66:67]
	v_lshlrev_b32_e32 v40, 16, v42
	v_and_b32_e32 v41, 0xffff0000, v42
	v_pk_fma_f32 v[36:37], v[48:49], v[40:41], v[36:37]
	v_lshlrev_b32_e32 v40, 16, v46
	v_and_b32_e32 v41, 0xffff0000, v46
	v_pk_mul_f32 v[48:49], v[136:137], v[94:95] op_sel_hi:[0,1]
	v_pk_fma_f32 v[36:37], v[48:49], v[40:41], v[36:37]
	v_lshlrev_b32_e32 v40, 16, v50
	v_and_b32_e32 v41, 0xffff0000, v50
	s_waitcnt vmcnt(0)
; __device__ __forceinline__ unsigned f2bf(float f) { unsigned u = __builtin_bit_cast(unsigned, f); return (u + 0x7fffu + ((u >> 16) & 1u)) >> 16; }
; DI unsigned pk2h(float lo, float hi) { const f32x2h_t v = {lo, hi}; return __builtin_bit_cast(unsigned, __builtin_convertvector(v, bf16x2h_t)); }
; DI float silu_f(float x) { return x * __builtin_amdgcn_rcpf(1.f + __expf(-x)); }
; DI void ssd_local_unit(Frame& F, int l, int ch, int g) {
;     ...
;         for (int cc = 0; cc < 4; ++cc) {
;             const int lc = cg * 32 + cc * 8, c0 = part * 256 + g * 128 + lc;
;             float acc[8];
;             { const f32x4 b0 = *(const f32x4*)(cb + c0), b1 = *(const f32x4*)(cb + c0 + 4);
; #pragma unroll
;               for (int e = 0; e < 4; ++e) { acc[e] = b0[e]; acc[4 + e] = b1[e]; } }
; #pragma unroll
;             for (int j = 0; j < 4; ++j) { float x[8]; unpack8(raw[cc][j], x);
;                 const f32x4 w0 = *(const f32x4*)(cw + j * XC + c0), w1 = *(const f32x4*)(cw + j * XC + c0 + 4);
; #pragma unroll
;                 for (int e = 0; e < 4; ++e) { acc[e] += w0[e] * okm[j] * x[e]; acc[4 + e] += w1[e] * okm[j] * x[4 + e]; } }
; #pragma unroll
;             for (int e = 0; e < 8; ++e) acc[e] = silu_f(acc[e]);
;             v4u o; o.x = pk2h(acc[0], acc[1]); o.y = pk2h(acc[2], acc[3]); o.z = pk2h(acc[4], acc[5]); o.w = pk2h(acc[6], acc[7]);
;             *(v4u*)(xbcc + (size_t)(t0 + s) * XC + c0) = o;
;             if (part == 0) { const int r2 = lc >> 6; const float dtv = DT[r2 * 128 + s], sc = dtv * __expf(AC[r2 * 128 + 127] - AC[r2 * 128 + s]);
; #pragma unroll
;                 for (int e = 0; e < 8; ++e) { XWT[(lc + e) * LP + s] = (bf16)f2bf(acc[e] * sc); XD[(lc + e) * LP + s] = (bf16)f2bf(acc[e] * dtv); } }
	v_pk_mul_f32 v[48:49], v[134:135], v[102:103] op_sel_hi:[0,1]
	v_pk_fma_f32 v[36:37], v[48:49], v[40:41], v[36:37]
	s_nop 0
	v_mul_f32_e32 v0, 0xbfb8aa3b, v36
	v_exp_f32_e32 v0, v0
	s_nop 0
	v_add_f32_e32 v0, 1.0, v0
	v_rcp_f32_e32 v40, v0
	v_mul_f32_e32 v0, 0xbfb8aa3b, v37
	v_exp_f32_e32 v0, v0
	s_nop 0
	v_add_f32_e32 v0, 1.0, v0
	v_rcp_f32_e32 v41, v0
	s_nop 0
	v_pk_mul_f32 v[48:49], v[36:37], v[40:41]
	v_lshlrev_b32_e32 v36, 16, v39
	v_and_b32_e32 v37, 0xffff0000, v39
	v_pk_mul_f32 v[38:39], v[140:141], v[76:77] op_sel_hi:[0,1]
	v_pk_fma_f32 v[36:37], v[38:39], v[36:37], v[68:69]
	v_lshlrev_b32_e32 v38, 16, v43
	v_and_b32_e32 v39, 0xffff0000, v43
	v_pk_mul_f32 v[40:41], v[138:139], v[84:85] op_sel_hi:[0,1]
	v_pk_fma_f32 v[36:37], v[40:41], v[38:39], v[36:37]
	v_lshlrev_b32_e32 v38, 16, v47
	v_and_b32_e32 v39, 0xffff0000, v47
	v_pk_mul_f32 v[40:41], v[136:137], v[96:97] op_sel_hi:[0,1]
	v_pk_fma_f32 v[36:37], v[40:41], v[38:39], v[36:37]
	v_lshlrev_b32_e32 v38, 16, v51
	v_and_b32_e32 v39, 0xffff0000, v51
	v_pk_mul_f32 v[40:41], v[134:135], v[104:105] op_sel_hi:[0,1]
	v_pk_fma_f32 v[36:37], v[40:41], v[38:39], v[36:37]
	v_lshl_add_u64 v[40:41], v[2:3], 1, v[142:143]
	v_mul_f32_e32 v0, 0xbfb8aa3b, v36
	v_exp_f32_e32 v0, v0
	v_lshl_add_u64 v[50:51], v[52:53], 0, s[0:1]
	s_mov_b64 s[0:1], 0x2440
	v_add_f32_e32 v0, 1.0, v0
	v_rcp_f32_e32 v38, v0
	v_mul_f32_e32 v0, 0xbfb8aa3b, v37
	v_exp_f32_e32 v0, v0
	s_nop 0
	v_add_f32_e32 v0, 1.0, v0
	v_rcp_f32_e32 v39, v0
	v_mul_f32_e32 v0, v61, v70
	v_bfe_u32 v2, v0, 16, 1
	v_add3_u32 v0, v0, v2, s97
	v_pk_mul_f32 v[42:43], v[36:37], v[38:39]
	v_mul_u32_u24_e32 v2, 0x88, v163
	v_cvt_pk_bf16_f32 v36, v70, v71
	v_cvt_pk_bf16_f32 v37, v44, v45
	v_cvt_pk_bf16_f32 v38, v48, v49
	v_cvt_pk_bf16_f32 v39, v42, v43
	v_lshlrev_b32_e32 v2, 1, v2
	global_store_dwordx4 v[40:41], v[36:39], off offset:16
	s_nop 1
	v_add_u32_e32 v36, v135, v2
	ds_write_b16_d16_hi v36, v0
	v_mul_f32_e32 v0, v60, v70
	v_bfe_u32 v36, v0, 16, 1
	v_add3_u32 v0, v0, v36, s97
	v_add_u32_e32 v2, v64, v2
	ds_write_b16_d16_hi v2, v0
	v_mul_f32_e32 v0, v61, v71
	v_bfe_u32 v2, v0, 16, 1
	v_add3_u32 v0, v0, v2, s97
	ds_write_b16_d16_hi v62, v0 offset:2448
	v_mul_f32_e32 v0, v60, v71
	v_bfe_u32 v2, v0, 16, 1
	v_add3_u32 v0, v0, v2, s97
	ds_write_b16_d16_hi v63, v0 offset:2448
	v_mul_f32_e32 v0, v61, v44
	v_bfe_u32 v2, v0, 16, 1
	v_add3_u32 v0, v0, v2, s97
	ds_write_b16_d16_hi v62, v0 offset:2720
	v_mul_f32_e32 v0, v60, v44
	v_bfe_u32 v2, v0, 16, 1
	v_add3_u32 v0, v0, v2, s97
	ds_write_b16_d16_hi v63, v0 offset:2720
	v_mul_f32_e32 v0, v61, v45
	v_bfe_u32 v2, v0, 16, 1
	v_add3_u32 v0, v0, v2, s97
	ds_write_b16_d16_hi v62, v0 offset:2992
	v_mul_f32_e32 v0, v60, v45
	v_bfe_u32 v2, v0, 16, 1
	v_add3_u32 v0, v0, v2, s97
	ds_write_b16_d16_hi v63, v0 offset:2992
	v_mul_f32_e32 v0, v61, v48
	v_bfe_u32 v2, v0, 16, 1
	v_add3_u32 v0, v0, v2, s97
	ds_write_b16_d16_hi v62, v0 offset:3264
	v_mul_f32_e32 v0, v60, v48
	v_bfe_u32 v2, v0, 16, 1
	v_add3_u32 v0, v0, v2, s97
	ds_write_b16_d16_hi v63, v0 offset:3264
	v_mul_f32_e32 v0, v61, v49
	v_bfe_u32 v2, v0, 16, 1
	v_add3_u32 v0, v0, v2, s97
	ds_write_b16_d16_hi v62, v0 offset:3536
	v_mul_f32_e32 v0, v60, v49
	v_bfe_u32 v2, v0, 16, 1
	v_add3_u32 v0, v0, v2, s97
	ds_write_b16_d16_hi v63, v0 offset:3536
	v_mul_f32_e32 v0, v61, v42
	v_bfe_u32 v2, v0, 16, 1
	v_add3_u32 v0, v0, v2, s97
	ds_write_b16_d16_hi v62, v0 offset:3808
	v_mul_f32_e32 v0, v60, v42
	v_bfe_u32 v2, v0, 16, 1
	v_add3_u32 v0, v0, v2, s97
	ds_write_b16_d16_hi v63, v0 offset:3808
	v_mul_f32_e32 v0, v61, v43
	v_bfe_u32 v2, v0, 16, 1
	v_add3_u32 v0, v0, v2, s97
	ds_write_b16_d16_hi v62, v0 offset:4080
	v_mul_f32_e32 v0, v60, v43
	v_bfe_u32 v2, v0, 16, 1
	v_add3_u32 v0, v0, v2, s97
	ds_write_b16_d16_hi v63, v0 offset:4080
	global_load_dwordx4 v[36:39], v[58:59], off offset:80
	global_load_dwordx4 v[42:45], v[58:59], off offset:64
	global_load_dwordx4 v[46:49], v[52:53], off offset:80
	global_load_dwordx4 v[66:69], v[52:53], off offset:64
	global_load_dwordx4 v[70:73], v[52:53], off offset:3152
	global_load_dwordx4 v[74:77], v[52:53], off offset:3136
	global_load_dwordx4 v[78:81], v[54:55], off offset:2112
	global_load_dwordx4 v[82:85], v[50:51], off offset:16
	v_lshl_add_u64 v[50:51], v[52:53], 0, s[0:1]
	global_load_dwordx4 v[86:89], v[56:57], off offset:1088
	global_load_dwordx4 v[90:93], v[50:51], off offset:16
	v_lshlrev_b32_e32 v50, 16, v20
	v_and_b32_e32 v51, 0xffff0000, v20
	v_lshlrev_b32_e32 v20, 16, v21
	v_and_b32_e32 v21, 0xffff0000, v21
	s_mov_b64 s[0:1], 0x1860
	s_waitcnt vmcnt(6)
	v_pk_mul_f32 v[66:67], v[140:141], v[66:67] op_sel_hi:[0,1]
	v_pk_fma_f32 v[42:43], v[66:67], v[50:51], v[42:43]
	v_lshlrev_b32_e32 v50, 16, v24
	v_and_b32_e32 v51, 0xffff0000, v24
	s_waitcnt vmcnt(4)
	v_pk_mul_f32 v[66:67], v[138:139], v[74:75] op_sel_hi:[0,1]
	v_pk_fma_f32 v[42:43], v[66:67], v[50:51], v[42:43]
	v_lshlrev_b32_e32 v50, 16, v28
	v_and_b32_e32 v51, 0xffff0000, v28
	s_waitcnt vmcnt(3)
	v_pk_mul_f32 v[66:67], v[136:137], v[78:79] op_sel_hi:[0,1]
	v_pk_fma_f32 v[42:43], v[66:67], v[50:51], v[42:43]
	v_lshlrev_b32_e32 v50, 16, v32
	v_and_b32_e32 v51, 0xffff0000, v32
	s_waitcnt vmcnt(1)
; __device__ __forceinline__ unsigned f2bf(float f) { unsigned u = __builtin_bit_cast(unsigned, f); return (u + 0x7fffu + ((u >> 16) & 1u)) >> 16; }
; DI unsigned pk2h(float lo, float hi) { const f32x2h_t v = {lo, hi}; return __builtin_bit_cast(unsigned, __builtin_convertvector(v, bf16x2h_t)); }
; DI float silu_f(float x) { return x * __builtin_amdgcn_rcpf(1.f + __expf(-x)); }
; DI void ssd_local_unit(Frame& F, int l, int ch, int g) {
;     ...
;         for (int cc = 0; cc < 4; ++cc) {
;             const int lc = cg * 32 + cc * 8, c0 = part * 256 + g * 128 + lc;
;             float acc[8];
;             { const f32x4 b0 = *(const f32x4*)(cb + c0), b1 = *(const f32x4*)(cb + c0 + 4);
; #pragma unroll
;               for (int e = 0; e < 4; ++e) { acc[e] = b0[e]; acc[4 + e] = b1[e]; } }
; #pragma unroll
;             for (int j = 0; j < 4; ++j) { float x[8]; unpack8(raw[cc][j], x);
;                 const f32x4 w0 = *(const f32x4*)(cw + j * XC + c0), w1 = *(const f32x4*)(cw + j * XC + c0 + 4);
; #pragma unroll
;                 for (int e = 0; e < 4; ++e) { acc[e] += w0[e] * okm[j] * x[e]; acc[4 + e] += w1[e] * okm[j] * x[4 + e]; } }
; #pragma unroll
;             for (int e = 0; e < 8; ++e) acc[e] = silu_f(acc[e]);
;             v4u o; o.x = pk2h(acc[0], acc[1]); o.y = pk2h(acc[2], acc[3]); o.z = pk2h(acc[4], acc[5]); o.w = pk2h(acc[6], acc[7]);
;             *(v4u*)(xbcc + (size_t)(t0 + s) * XC + c0) = o;
;             if (part == 0) { const int r2 = lc >> 6; const float dtv = DT[r2 * 128 + s], sc = dtv * __expf(AC[r2 * 128 + 127] - AC[r2 * 128 + s]);
; #pragma unroll
;                 for (int e = 0; e < 8; ++e) { XWT[(lc + e) * LP + s] = (bf16)f2bf(acc[e] * sc); XD[(lc + e) * LP + s] = (bf16)f2bf(acc[e] * dtv); } }
	v_pk_mul_f32 v[66:67], v[134:135], v[86:87] op_sel_hi:[0,1]
	v_pk_fma_f32 v[42:43], v[66:67], v[50:51], v[42:43]
	v_lshlrev_b32_e32 v24, 16, v25
	v_mul_f32_e32 v0, 0xbfb8aa3b, v42
	v_exp_f32_e32 v0, v0
	v_and_b32_e32 v25, 0xffff0000, v25
	v_add_f32_e32 v0, 1.0, v0
	v_rcp_f32_e32 v50, v0
	v_mul_f32_e32 v0, 0xbfb8aa3b, v43
	v_exp_f32_e32 v0, v0
	s_nop 0
	v_add_f32_e32 v0, 1.0, v0
	v_rcp_f32_e32 v51, v0
	s_nop 0
	v_pk_mul_f32 v[42:43], v[42:43], v[50:51]
	v_pk_mul_f32 v[50:51], v[140:141], v[68:69] op_sel_hi:[0,1]
	v_pk_fma_f32 v[20:21], v[50:51], v[20:21], v[44:45]
	v_pk_mul_f32 v[44:45], v[138:139], v[76:77] op_sel_hi:[0,1]
	v_pk_fma_f32 v[20:21], v[44:45], v[24:25], v[20:21]
	v_lshlrev_b32_e32 v24, 16, v29
	v_and_b32_e32 v25, 0xffff0000, v29
	v_pk_mul_f32 v[28:29], v[136:137], v[80:81] op_sel_hi:[0,1]
	v_pk_fma_f32 v[20:21], v[28:29], v[24:25], v[20:21]
	v_lshlrev_b32_e32 v24, 16, v33
	v_and_b32_e32 v25, 0xffff0000, v33
	v_pk_mul_f32 v[28:29], v[134:135], v[88:89] op_sel_hi:[0,1]
	v_pk_fma_f32 v[20:21], v[28:29], v[24:25], v[20:21]
	v_pk_mul_f32 v[28:29], v[140:141], v[46:47] op_sel_hi:[0,1]
	v_mul_f32_e32 v0, 0xbfb8aa3b, v20
	v_exp_f32_e32 v0, v0
	v_pk_mul_f32 v[32:33], v[138:139], v[70:71] op_sel_hi:[0,1]
	v_lshl_add_u64 v[50:51], v[52:53], 0, s[0:1]
	s_mov_b64 s[0:1], 0x2460
	v_add_f32_e32 v0, 1.0, v0
	v_rcp_f32_e32 v24, v0
	v_mul_f32_e32 v0, 0xbfb8aa3b, v21
	v_exp_f32_e32 v0, v0
	s_nop 0
	v_add_f32_e32 v0, 1.0, v0
	v_rcp_f32_e32 v25, v0
	s_nop 0
	v_pk_mul_f32 v[24:25], v[20:21], v[24:25]
	v_lshlrev_b32_e32 v20, 16, v22
	v_and_b32_e32 v21, 0xffff0000, v22
	v_pk_fma_f32 v[20:21], v[28:29], v[20:21], v[36:37]
	v_lshlrev_b32_e32 v28, 16, v26
	v_and_b32_e32 v29, 0xffff0000, v26
	v_pk_fma_f32 v[20:21], v[32:33], v[28:29], v[20:21]
	v_lshlrev_b32_e32 v28, 16, v30
	v_and_b32_e32 v29, 0xffff0000, v30
	v_pk_mul_f32 v[32:33], v[136:137], v[82:83] op_sel_hi:[0,1]
	v_pk_fma_f32 v[20:21], v[32:33], v[28:29], v[20:21]
	v_lshlrev_b32_e32 v28, 16, v34
	v_and_b32_e32 v29, 0xffff0000, v34
	s_waitcnt vmcnt(0)
	v_pk_mul_f32 v[32:33], v[134:135], v[90:91] op_sel_hi:[0,1]
	v_pk_fma_f32 v[20:21], v[32:33], v[28:29], v[20:21]
	s_nop 0
	v_mul_f32_e32 v0, 0xbfb8aa3b, v20
	v_exp_f32_e32 v0, v0
	s_nop 0
	v_add_f32_e32 v0, 1.0, v0
	v_rcp_f32_e32 v28, v0
	v_mul_f32_e32 v0, 0xbfb8aa3b, v21
	v_exp_f32_e32 v0, v0
	s_nop 0
	v_add_f32_e32 v0, 1.0, v0
	v_rcp_f32_e32 v29, v0
	s_nop 0
	v_pk_mul_f32 v[28:29], v[20:21], v[28:29]
	v_lshlrev_b32_e32 v20, 16, v23
	v_and_b32_e32 v21, 0xffff0000, v23
	v_pk_mul_f32 v[22:23], v[140:141], v[48:49] op_sel_hi:[0,1]
	v_pk_fma_f32 v[20:21], v[22:23], v[20:21], v[38:39]
	v_lshlrev_b32_e32 v22, 16, v27
	v_and_b32_e32 v23, 0xffff0000, v27
	v_pk_mul_f32 v[26:27], v[138:139], v[72:73] op_sel_hi:[0,1]
	v_pk_fma_f32 v[20:21], v[26:27], v[22:23], v[20:21]
	v_lshlrev_b32_e32 v22, 16, v31
	v_and_b32_e32 v23, 0xffff0000, v31
	v_pk_mul_f32 v[26:27], v[136:137], v[84:85] op_sel_hi:[0,1]
	v_pk_fma_f32 v[20:21], v[26:27], v[22:23], v[20:21]
	v_lshlrev_b32_e32 v22, 16, v35
	v_and_b32_e32 v23, 0xffff0000, v35
	v_pk_mul_f32 v[26:27], v[134:135], v[92:93] op_sel_hi:[0,1]
	v_pk_fma_f32 v[20:21], v[26:27], v[22:23], v[20:21]
	s_nop 0
	v_mul_f32_e32 v0, 0xbfb8aa3b, v20
	v_exp_f32_e32 v0, v0
	s_nop 0
	v_add_f32_e32 v0, 1.0, v0
	v_rcp_f32_e32 v22, v0
	v_mul_f32_e32 v0, 0xbfb8aa3b, v21
	v_exp_f32_e32 v0, v0
	s_nop 0
	v_add_f32_e32 v0, 1.0, v0
	v_rcp_f32_e32 v23, v0
	v_mul_f32_e32 v0, v61, v42
	v_bfe_u32 v2, v0, 16, 1
	v_add3_u32 v0, v0, v2, s97
	v_pk_mul_f32 v[26:27], v[20:21], v[22:23]
	v_mul_u32_u24_e32 v2, 0x88, v162
	v_cvt_pk_bf16_f32 v20, v42, v43
	v_cvt_pk_bf16_f32 v21, v24, v25
	v_cvt_pk_bf16_f32 v22, v28, v29
	v_cvt_pk_bf16_f32 v23, v26, v27
	v_lshlrev_b32_e32 v2, 1, v2
	global_store_dwordx4 v[40:41], v[20:23], off offset:32
	s_nop 1
	v_add_u32_e32 v20, v135, v2
	ds_write_b16_d16_hi v20, v0
	v_mul_f32_e32 v0, v60, v42
	v_bfe_u32 v20, v0, 16, 1
	v_add3_u32 v0, v0, v20, s97
	v_add_u32_e32 v2, v64, v2
	ds_write_b16_d16_hi v2, v0
	v_mul_f32_e32 v0, v61, v43
	v_bfe_u32 v2, v0, 16, 1
	v_add3_u32 v0, v0, v2, s97
	ds_write_b16_d16_hi v62, v0 offset:4624
	v_mul_f32_e32 v0, v60, v43
	v_bfe_u32 v2, v0, 16, 1
	v_add3_u32 v0, v0, v2, s97
	ds_write_b16_d16_hi v63, v0 offset:4624
	v_mul_f32_e32 v0, v61, v24
	v_bfe_u32 v2, v0, 16, 1
	v_add3_u32 v0, v0, v2, s97
	ds_write_b16_d16_hi v62, v0 offset:4896
	v_mul_f32_e32 v0, v60, v24
	v_bfe_u32 v2, v0, 16, 1
	v_add3_u32 v0, v0, v2, s97
	ds_write_b16_d16_hi v63, v0 offset:4896
	v_mul_f32_e32 v0, v61, v25
	v_bfe_u32 v2, v0, 16, 1
	v_add3_u32 v0, v0, v2, s97
	ds_write_b16_d16_hi v62, v0 offset:5168
	v_mul_f32_e32 v0, v60, v25
	v_bfe_u32 v2, v0, 16, 1
	v_add3_u32 v0, v0, v2, s97
	ds_write_b16_d16_hi v63, v0 offset:5168
	v_mul_f32_e32 v0, v61, v28
	v_bfe_u32 v2, v0, 16, 1
	v_add3_u32 v0, v0, v2, s97
	ds_write_b16_d16_hi v62, v0 offset:5440
	v_mul_f32_e32 v0, v60, v28
	v_bfe_u32 v2, v0, 16, 1
	v_add3_u32 v0, v0, v2, s97
	ds_write_b16_d16_hi v63, v0 offset:5440
	v_mul_f32_e32 v0, v61, v29
	v_bfe_u32 v2, v0, 16, 1
	v_add3_u32 v0, v0, v2, s97
	ds_write_b16_d16_hi v62, v0 offset:5712
	v_mul_f32_e32 v0, v60, v29
	v_bfe_u32 v2, v0, 16, 1
	v_add3_u32 v0, v0, v2, s97
	ds_write_b16_d16_hi v63, v0 offset:5712
	v_mul_f32_e32 v0, v61, v26
	v_bfe_u32 v2, v0, 16, 1
	v_add3_u32 v0, v0, v2, s97
	ds_write_b16_d16_hi v62, v0 offset:5984
	v_mul_f32_e32 v0, v60, v26
	v_bfe_u32 v2, v0, 16, 1
	v_add3_u32 v0, v0, v2, s97
	ds_write_b16_d16_hi v63, v0 offset:5984
	v_mul_f32_e32 v0, v61, v27
	v_bfe_u32 v2, v0, 16, 1
	v_add3_u32 v0, v0, v2, s97
	ds_write_b16_d16_hi v62, v0 offset:6256
	v_mul_f32_e32 v0, v60, v27
	v_bfe_u32 v2, v0, 16, 1
	v_add3_u32 v0, v0, v2, s97
	ds_write_b16_d16_hi v63, v0 offset:6256
	global_load_dwordx4 v[20:23], v[58:59], off offset:112
	global_load_dwordx4 v[24:27], v[58:59], off offset:96
	global_load_dwordx4 v[28:31], v[52:53], off offset:112
	global_load_dwordx4 v[32:35], v[52:53], off offset:96
	global_load_dwordx4 v[36:39], v[52:53], off offset:3184
	global_load_dwordx4 v[42:45], v[52:53], off offset:3168
	global_load_dwordx4 v[46:49], v[54:55], off offset:2144
	global_load_dwordx4 v[66:69], v[50:51], off offset:16
	v_lshl_add_u64 v[54:55], v[52:53], 0, s[0:1]
	global_load_dwordx4 v[50:53], v[56:57], off offset:1120
	s_nop 0
	global_load_dwordx4 v[54:57], v[54:55], off offset:16
	v_lshlrev_b32_e32 v58, 16, v4
	v_and_b32_e32 v59, 0xffff0000, v4
	v_lshlrev_b32_e32 v4, 16, v5
	v_and_b32_e32 v5, 0xffff0000, v5
	s_waitcnt vmcnt(6)
; #define LAS __attribute__((address_space(3)))
; __device__ __forceinline__ unsigned f2bf(float f) { unsigned u = __builtin_bit_cast(unsigned, f); return (u + 0x7fffu + ((u >> 16) & 1u)) >> 16; }
; DI unsigned pk2h(float lo, float hi) { const f32x2h_t v = {lo, hi}; return __builtin_bit_cast(unsigned, __builtin_convertvector(v, bf16x2h_t)); }
; DI float silu_f(float x) { return x * __builtin_amdgcn_rcpf(1.f + __expf(-x)); }
; DI void ssd_local_unit(Frame& F, int l, int ch, int g) {
;     ...
;         for (int cc = 0; cc < 4; ++cc) {
;             const int lc = cg * 32 + cc * 8, c0 = part * 256 + g * 128 + lc;
;             float acc[8];
;             { const f32x4 b0 = *(const f32x4*)(cb + c0), b1 = *(const f32x4*)(cb + c0 + 4);
; #pragma unroll
;               for (int e = 0; e < 4; ++e) { acc[e] = b0[e]; acc[4 + e] = b1[e]; } }
; #pragma unroll
;             for (int j = 0; j < 4; ++j) { float x[8]; unpack8(raw[cc][j], x);
;                 const f32x4 w0 = *(const f32x4*)(cw + j * XC + c0), w1 = *(const f32x4*)(cw + j * XC + c0 + 4);
; #pragma unroll
;                 for (int e = 0; e < 4; ++e) { acc[e] += w0[e] * okm[j] * x[e]; acc[4 + e] += w1[e] * okm[j] * x[4 + e]; } }
; #pragma unroll
;             for (int e = 0; e < 8; ++e) acc[e] = silu_f(acc[e]);
;             v4u o; o.x = pk2h(acc[0], acc[1]); o.y = pk2h(acc[2], acc[3]); o.z = pk2h(acc[4], acc[5]); o.w = pk2h(acc[6], acc[7]);
;             *(v4u*)(xbcc + (size_t)(t0 + s) * XC + c0) = o;
;             if (part == 0) { const int r2 = lc >> 6; const float dtv = DT[r2 * 128 + s], sc = dtv * __expf(AC[r2 * 128 + 127] - AC[r2 * 128 + s]);
; #pragma unroll
;                 for (int e = 0; e < 8; ++e) { XWT[(lc + e) * LP + s] = (bf16)f2bf(acc[e] * sc); XD[(lc + e) * LP + s] = (bf16)f2bf(acc[e] * dtv); } }
;     ...
;     __syncthreads();
;     const int w = F.wave, r = F.lane & 15, q = F.lane >> 4;
;     f32x4 acc[8];
; #pragma unroll
;     for (int nt = 0; nt < 8; ++nt) acc[nt] = (f32x4){0.f, 0.f, 0.f, 0.f};
; #pragma unroll
;     for (int ks = 0; ks < 4; ++ks) { const bf16x8 a = *(const LAS bf16x8*)(XWT + (16 * w + r) * LP + 32 * ks + 8 * q);
	v_pk_mul_f32 v[32:33], v[140:141], v[32:33] op_sel_hi:[0,1]
	v_pk_fma_f32 v[24:25], v[32:33], v[58:59], v[24:25]
	v_lshlrev_b32_e32 v32, 16, v8
	v_and_b32_e32 v33, 0xffff0000, v8
	s_waitcnt vmcnt(4)
	v_pk_mul_f32 v[42:43], v[138:139], v[42:43] op_sel_hi:[0,1]
	v_pk_fma_f32 v[24:25], v[42:43], v[32:33], v[24:25]
	v_lshlrev_b32_e32 v32, 16, v12
	v_and_b32_e32 v33, 0xffff0000, v12
	s_waitcnt vmcnt(3)
	v_pk_mul_f32 v[42:43], v[136:137], v[46:47] op_sel_hi:[0,1]
	v_pk_fma_f32 v[24:25], v[42:43], v[32:33], v[24:25]
	v_lshlrev_b32_e32 v32, 16, v16
	v_and_b32_e32 v33, 0xffff0000, v16
	s_waitcnt vmcnt(1)
	v_pk_mul_f32 v[42:43], v[134:135], v[50:51] op_sel_hi:[0,1]
	v_pk_fma_f32 v[24:25], v[42:43], v[32:33], v[24:25]
	v_lshlrev_b32_e32 v8, 16, v9
	v_mul_f32_e32 v0, 0xbfb8aa3b, v24
	v_exp_f32_e32 v0, v0
	v_and_b32_e32 v9, 0xffff0000, v9
	v_add_f32_e32 v0, 1.0, v0
	v_rcp_f32_e32 v32, v0
	v_mul_f32_e32 v0, 0xbfb8aa3b, v25
	v_exp_f32_e32 v0, v0
	s_nop 0
	v_add_f32_e32 v0, 1.0, v0
	v_rcp_f32_e32 v33, v0
	s_nop 0
	v_pk_mul_f32 v[24:25], v[24:25], v[32:33]
	v_pk_mul_f32 v[32:33], v[140:141], v[34:35] op_sel_hi:[0,1]
	v_pk_fma_f32 v[4:5], v[32:33], v[4:5], v[26:27]
	v_pk_mul_f32 v[26:27], v[138:139], v[44:45] op_sel_hi:[0,1]
	v_pk_fma_f32 v[4:5], v[26:27], v[8:9], v[4:5]
	v_lshlrev_b32_e32 v8, 16, v13
	v_and_b32_e32 v9, 0xffff0000, v13
	v_pk_mul_f32 v[12:13], v[136:137], v[48:49] op_sel_hi:[0,1]
	v_pk_fma_f32 v[4:5], v[12:13], v[8:9], v[4:5]
	v_lshlrev_b32_e32 v8, 16, v17
	v_and_b32_e32 v9, 0xffff0000, v17
	v_pk_mul_f32 v[12:13], v[134:135], v[52:53] op_sel_hi:[0,1]
	v_pk_fma_f32 v[4:5], v[12:13], v[8:9], v[4:5]
	v_pk_mul_f32 v[12:13], v[140:141], v[28:29] op_sel_hi:[0,1]
	v_mul_f32_e32 v0, 0xbfb8aa3b, v4
	v_exp_f32_e32 v0, v0
	v_pk_mul_f32 v[16:17], v[138:139], v[36:37] op_sel_hi:[0,1]
	v_add_f32_e32 v0, 1.0, v0
	v_rcp_f32_e32 v8, v0
	v_mul_f32_e32 v0, 0xbfb8aa3b, v5
	v_exp_f32_e32 v0, v0
	s_nop 0
	v_add_f32_e32 v0, 1.0, v0
	v_rcp_f32_e32 v9, v0
	s_nop 0
	v_pk_mul_f32 v[8:9], v[4:5], v[8:9]
	v_lshlrev_b32_e32 v4, 16, v6
	v_and_b32_e32 v5, 0xffff0000, v6
	v_pk_fma_f32 v[4:5], v[12:13], v[4:5], v[20:21]
	v_lshlrev_b32_e32 v12, 16, v10
	v_and_b32_e32 v13, 0xffff0000, v10
	v_pk_fma_f32 v[4:5], v[16:17], v[12:13], v[4:5]
	v_lshlrev_b32_e32 v12, 16, v14
	v_and_b32_e32 v13, 0xffff0000, v14
	v_pk_mul_f32 v[16:17], v[136:137], v[66:67] op_sel_hi:[0,1]
	v_pk_fma_f32 v[4:5], v[16:17], v[12:13], v[4:5]
	v_lshlrev_b32_e32 v12, 16, v18
	v_and_b32_e32 v13, 0xffff0000, v18
	s_waitcnt vmcnt(0)
	v_pk_mul_f32 v[16:17], v[134:135], v[54:55] op_sel_hi:[0,1]
	v_pk_fma_f32 v[4:5], v[16:17], v[12:13], v[4:5]
	s_nop 0
	v_mul_f32_e32 v0, 0xbfb8aa3b, v4
	v_exp_f32_e32 v0, v0
	s_nop 0
	v_add_f32_e32 v0, 1.0, v0
	v_rcp_f32_e32 v12, v0
	v_mul_f32_e32 v0, 0xbfb8aa3b, v5
	v_exp_f32_e32 v0, v0
	s_nop 0
	v_add_f32_e32 v0, 1.0, v0
	v_rcp_f32_e32 v13, v0
	s_nop 0
	v_pk_mul_f32 v[12:13], v[4:5], v[12:13]
	v_lshlrev_b32_e32 v4, 16, v7
	v_and_b32_e32 v5, 0xffff0000, v7
	v_pk_mul_f32 v[6:7], v[140:141], v[30:31] op_sel_hi:[0,1]
	v_pk_fma_f32 v[4:5], v[6:7], v[4:5], v[22:23]
	v_lshlrev_b32_e32 v6, 16, v11
	v_and_b32_e32 v7, 0xffff0000, v11
	v_pk_mul_f32 v[10:11], v[138:139], v[38:39] op_sel_hi:[0,1]
	v_pk_fma_f32 v[4:5], v[10:11], v[6:7], v[4:5]
	v_lshlrev_b32_e32 v6, 16, v15
	v_and_b32_e32 v7, 0xffff0000, v15
	v_pk_mul_f32 v[10:11], v[136:137], v[68:69] op_sel_hi:[0,1]
	v_pk_fma_f32 v[4:5], v[10:11], v[6:7], v[4:5]
	v_lshlrev_b32_e32 v6, 16, v19
	v_and_b32_e32 v7, 0xffff0000, v19
	v_pk_mul_f32 v[10:11], v[134:135], v[56:57] op_sel_hi:[0,1]
	v_pk_fma_f32 v[4:5], v[10:11], v[6:7], v[4:5]
	s_nop 0
	v_mul_f32_e32 v0, 0xbfb8aa3b, v4
	v_exp_f32_e32 v0, v0
	s_nop 0
	v_add_f32_e32 v0, 1.0, v0
	v_rcp_f32_e32 v6, v0
	v_mul_f32_e32 v0, 0xbfb8aa3b, v5
	v_exp_f32_e32 v0, v0
	s_nop 0
	v_add_f32_e32 v0, 1.0, v0
	v_rcp_f32_e32 v7, v0
	v_mul_f32_e32 v0, v61, v24
	v_bfe_u32 v2, v0, 16, 1
	v_add3_u32 v0, v0, v2, s97
	v_pk_mul_f32 v[10:11], v[4:5], v[6:7]
	v_mul_u32_u24_e32 v2, 0x88, v139
	v_cvt_pk_bf16_f32 v4, v24, v25
	v_cvt_pk_bf16_f32 v5, v8, v9
	v_cvt_pk_bf16_f32 v6, v12, v13
	v_cvt_pk_bf16_f32 v7, v10, v11
	v_lshlrev_b32_e32 v2, 1, v2
	global_store_dwordx4 v[40:41], v[4:7], off offset:48
	s_nop 1
	v_add_u32_e32 v4, v135, v2
	ds_write_b16_d16_hi v4, v0
	v_mul_f32_e32 v0, v60, v24
	v_bfe_u32 v4, v0, 16, 1
	v_add3_u32 v0, v0, v4, s97
	v_add_u32_e32 v2, v64, v2
	ds_write_b16_d16_hi v2, v0
	v_mul_f32_e32 v0, v61, v25
	v_bfe_u32 v2, v0, 16, 1
	v_add3_u32 v0, v0, v2, s97
	ds_write_b16_d16_hi v62, v0 offset:6800
	v_mul_f32_e32 v0, v60, v25
	v_bfe_u32 v2, v0, 16, 1
	v_add3_u32 v0, v0, v2, s97
	ds_write_b16_d16_hi v63, v0 offset:6800
	v_mul_f32_e32 v0, v61, v8
	v_bfe_u32 v2, v0, 16, 1
	v_add3_u32 v0, v0, v2, s97
	ds_write_b16_d16_hi v62, v0 offset:7072
	v_mul_f32_e32 v0, v60, v8
	v_bfe_u32 v2, v0, 16, 1
	v_add3_u32 v0, v0, v2, s97
	ds_write_b16_d16_hi v63, v0 offset:7072
	v_mul_f32_e32 v0, v61, v9
	v_bfe_u32 v2, v0, 16, 1
	v_add3_u32 v0, v0, v2, s97
	ds_write_b16_d16_hi v62, v0 offset:7344
	v_mul_f32_e32 v0, v60, v9
	v_bfe_u32 v2, v0, 16, 1
	v_add3_u32 v0, v0, v2, s97
	ds_write_b16_d16_hi v63, v0 offset:7344
	v_mul_f32_e32 v0, v61, v12
	v_bfe_u32 v2, v0, 16, 1
	v_add3_u32 v0, v0, v2, s97
	ds_write_b16_d16_hi v62, v0 offset:7616
	v_mul_f32_e32 v0, v60, v12
	v_bfe_u32 v2, v0, 16, 1
	v_add3_u32 v0, v0, v2, s97
	ds_write_b16_d16_hi v63, v0 offset:7616
	v_mul_f32_e32 v0, v61, v13
	v_bfe_u32 v2, v0, 16, 1
	v_add3_u32 v0, v0, v2, s97
	ds_write_b16_d16_hi v62, v0 offset:7888
	v_mul_f32_e32 v0, v60, v13
	v_bfe_u32 v2, v0, 16, 1
	v_add3_u32 v0, v0, v2, s97
	ds_write_b16_d16_hi v63, v0 offset:7888
	v_mul_f32_e32 v0, v61, v10
	v_bfe_u32 v2, v0, 16, 1
	v_add3_u32 v0, v0, v2, s97
	ds_write_b16_d16_hi v62, v0 offset:8160
	v_mul_f32_e32 v0, v60, v10
	v_bfe_u32 v2, v0, 16, 1
	v_add3_u32 v0, v0, v2, s97
	ds_write_b16_d16_hi v63, v0 offset:8160
	v_mul_f32_e32 v0, v61, v11
	v_bfe_u32 v2, v0, 16, 1
	v_add3_u32 v0, v0, v2, s97
	ds_write_b16_d16_hi v62, v0 offset:8432
	v_mul_f32_e32 v0, v60, v11
	v_bfe_u32 v2, v0, 16, 1
	v_add3_u32 v0, v0, v2, s97
	ds_write_b16_d16_hi v63, v0 offset:8432
	v_and_b32_e32 v2, 15, v132
	v_and_b32_e32 v0, 48, v133
	v_lshl_or_b32 v4, s37, 4, v2
	v_add_u32_e32 v0, s19, v0
	v_mad_u64_u32 v[48:49], s[0:1], v4, s66, v[0:1]
	v_mad_u32_u24 v0, v2, s66, v0
	s_waitcnt lgkmcnt(0)
	s_barrier
; #define LAS __attribute__((address_space(3)))
; DI f32x4 mfma16(bf16x8 a, bf16x8 b, f32x4 c) { asm volatile("s_nop 3" : "+v"(a), "+v"(b)); return __builtin_amdgcn_mfma_f32_16x16x32_bf16(a, b, c, 0, 0, 0); }
; DI void ssd_local_unit(Frame& F, int l, int ch, int g) {
;     ...
;     const int w = F.wave, r = F.lane & 15, q = F.lane >> 4;
;     f32x4 acc[8];
; #pragma unroll
;     for (int nt = 0; nt < 8; ++nt) acc[nt] = (f32x4){0.f, 0.f, 0.f, 0.f};
; #pragma unroll
;     for (int ks = 0; ks < 4; ++ks) { const bf16x8 a = *(const LAS bf16x8*)(XWT + (16 * w + r) * LP + 32 * ks + 8 * q);
; #pragma unroll
;         for (int nt = 0; nt < 8; ++nt) { const bf16x8 b = *(const LAS bf16x8*)(BT + (16 * nt + r) * LP + 32 * ks + 8 * q); acc[nt] = mfma16(a, b, acc[nt]); } }
	ds_read_b128 v[4:7], v0 offset:34816
	ds_read_b128 v[8:11], v48
	s_ashr_i32 s0, s38, 8
	s_add_i32 s0, s0, s2
	s_ashr_i32 s1, s0, 31
	s_lshl_b64 s[0:1], s[0:1], 15
	s_waitcnt lgkmcnt(0)
	v_mov_b64_e32 v[14:15], v[10:11]
	v_mov_b64_e32 v[12:13], v[8:9]
	s_nop 3
	v_mov_b64_e32 v[18:19], v[10:11]
	v_mov_b64_e32 v[16:17], v[8:9]
	v_mfma_f32_16x16x32_bf16 v[4:7], v[4:7], v[12:15], 0
	ds_read_b128 v[12:15], v0 offset:39168
	s_waitcnt lgkmcnt(0)
	s_nop 3
	v_mov_b64_e32 v[22:23], v[10:11]
	v_mfma_f32_16x16x32_bf16 v[12:15], v[12:15], v[16:19], 0
	ds_read_b128 v[16:19], v0 offset:43520
	v_mov_b64_e32 v[20:21], v[8:9]
	s_waitcnt lgkmcnt(0)
	s_nop 3
	v_mov_b64_e32 v[26:27], v[10:11]
	v_mov_b64_e32 v[24:25], v[8:9]
	v_mfma_f32_16x16x32_bf16 v[16:19], v[16:19], v[20:23], 0
	ds_read_b128 v[20:23], v0 offset:47872
	s_waitcnt lgkmcnt(0)
	s_nop 3
	v_mov_b64_e32 v[30:31], v[10:11]
	v_mfma_f32_16x16x32_bf16 v[20:23], v[20:23], v[24:27], 0
	ds_read_b128 v[24:27], v0 offset:52224
	v_mov_b64_e32 v[28:29], v[8:9]
	s_waitcnt lgkmcnt(0)
	s_nop 3
	v_mov_b64_e32 v[34:35], v[10:11]
	v_mov_b64_e32 v[32:33], v[8:9]
	v_mfma_f32_16x16x32_bf16 v[24:27], v[24:27], v[28:31], 0
	ds_read_b128 v[28:31], v0 offset:56576
	s_waitcnt lgkmcnt(0)
	s_nop 3
	v_mov_b64_e32 v[38:39], v[10:11]
	v_mfma_f32_16x16x32_bf16 v[28:31], v[28:31], v[32:35], 0
	ds_read_b128 v[32:35], v0 offset:60928
	v_mov_b64_e32 v[36:37], v[8:9]
	s_waitcnt lgkmcnt(0)
	s_nop 3
	s_add_u32 s0, s20, s0
	s_addc_u32 s1, s21, s1
	v_mfma_f32_16x16x32_bf16 v[32:35], v[32:35], v[36:39], 0
	ds_read_b128 v[36:39], v0 offset:65280
	s_waitcnt lgkmcnt(0)
	s_nop 3
	v_lshlrev_b32_e32 v2, 2, v2
	v_mfma_f32_16x16x32_bf16 v[8:11], v[36:39], v[8:11], 0
	ds_read_b128 v[36:39], v0 offset:34880
	ds_read_b128 v[40:43], v48 offset:64
	s_waitcnt lgkmcnt(0)
	v_mov_b64_e32 v[46:47], v[42:43]
	v_mov_b64_e32 v[44:45], v[40:41]
	s_nop 3
	s_nop 1
	v_mfma_f32_16x16x32_bf16 v[4:7], v[36:39], v[44:47], v[4:7]
	v_mov_b64_e32 v[46:47], v[42:43]
	ds_read_b128 v[36:39], v0 offset:39232
	v_mov_b64_e32 v[44:45], v[40:41]
	s_waitcnt lgkmcnt(0)
	s_nop 3
	s_nop 0
	v_mfma_f32_16x16x32_bf16 v[12:15], v[36:39], v[44:47], v[12:15]
	v_mov_b64_e32 v[46:47], v[42:43]
	ds_read_b128 v[36:39], v0 offset:43584
	v_mov_b64_e32 v[44:45], v[40:41]
	s_waitcnt lgkmcnt(0)
	s_nop 3
	s_nop 0
	v_mfma_f32_16x16x32_bf16 v[16:19], v[36:39], v[44:47], v[16:19]
	v_mov_b64_e32 v[46:47], v[42:43]
	ds_read_b128 v[36:39], v0 offset:47936
	v_mov_b64_e32 v[44:45], v[40:41]
	s_waitcnt lgkmcnt(0)
	s_nop 3
	s_nop 0
	v_mfma_f32_16x16x32_bf16 v[20:23], v[36:39], v[44:47], v[20:23]
	v_mov_b64_e32 v[46:47], v[42:43]
	ds_read_b128 v[36:39], v0 offset:52288
	v_mov_b64_e32 v[44:45], v[40:41]
	s_waitcnt lgkmcnt(0)
	s_nop 3
	s_nop 0
	v_mfma_f32_16x16x32_bf16 v[24:27], v[36:39], v[44:47], v[24:27]
	v_mov_b64_e32 v[46:47], v[42:43]
	ds_read_b128 v[36:39], v0 offset:56640
	v_mov_b64_e32 v[44:45], v[40:41]
	s_waitcnt lgkmcnt(0)
	s_nop 3
	s_nop 0
	v_mfma_f32_16x16x32_bf16 v[28:31], v[36:39], v[44:47], v[28:31]
	v_mov_b64_e32 v[46:47], v[42:43]
	ds_read_b128 v[36:39], v0 offset:60992
	v_mov_b64_e32 v[44:45], v[40:41]
	s_waitcnt lgkmcnt(0)
	s_nop 3
	s_nop 0
	v_mfma_f32_16x16x32_bf16 v[32:35], v[36:39], v[44:47], v[32:35]
	ds_read_b128 v[36:39], v0 offset:65344
	s_waitcnt lgkmcnt(0)
	s_nop 3
	s_nop 0
	v_mfma_f32_16x16x32_bf16 v[8:11], v[36:39], v[40:43], v[8:11]
	ds_read_b128 v[36:39], v0 offset:34944
	ds_read_b128 v[40:43], v48 offset:128
	s_waitcnt lgkmcnt(0)
	v_mov_b64_e32 v[46:47], v[42:43]
	v_mov_b64_e32 v[44:45], v[40:41]
	s_nop 3
	s_nop 1
	v_mfma_f32_16x16x32_bf16 v[4:7], v[36:39], v[44:47], v[4:7]
	v_mov_b64_e32 v[46:47], v[42:43]
	ds_read_b128 v[36:39], v0 offset:39296
	v_mov_b64_e32 v[44:45], v[40:41]
	s_waitcnt lgkmcnt(0)
	s_nop 3
	s_nop 0
	v_mfma_f32_16x16x32_bf16 v[12:15], v[36:39], v[44:47], v[12:15]
	v_mov_b64_e32 v[46:47], v[42:43]
	ds_read_b128 v[36:39], v0 offset:43648
	v_mov_b64_e32 v[44:45], v[40:41]
	s_waitcnt lgkmcnt(0)
	s_nop 3
	s_nop 0
	v_mfma_f32_16x16x32_bf16 v[16:19], v[36:39], v[44:47], v[16:19]
	v_mov_b64_e32 v[46:47], v[42:43]
	ds_read_b128 v[36:39], v0 offset:48000
	v_mov_b64_e32 v[44:45], v[40:41]
	s_waitcnt lgkmcnt(0)
; #define LAS __attribute__((address_space(3)))
; DI f32x4 mfma16(bf16x8 a, bf16x8 b, f32x4 c) { asm volatile("s_nop 3" : "+v"(a), "+v"(b)); return __builtin_amdgcn_mfma_f32_16x16x32_bf16(a, b, c, 0, 0, 0); }
; DI void ssd_local_unit(Frame& F, int l, int ch, int g) {
;     ...
; #pragma unroll
;     for (int ks = 0; ks < 4; ++ks) { const bf16x8 a = *(const LAS bf16x8*)(XWT + (16 * w + r) * LP + 32 * ks + 8 * q);
; #pragma unroll
;         for (int nt = 0; nt < 8; ++nt) { const bf16x8 b = *(const LAS bf16x8*)(BT + (16 * nt + r) * LP + 32 * ks + 8 * q); acc[nt] = mfma16(a, b, acc[nt]); } }
;     float* sst = (float*)(F.ws + WS_SST);
; #pragma unroll
;     for (int jj = 0; jj < 4; ++jj) { const int row = 16 * w + 4 * q + jj, head = 2 * g + (row >> 6), p = row & 63;
;         float* o = sst + ((size_t)(ch * 4 + head) * 64 + p) * 128 + r;
; #pragma unroll
;         for (int nt = 0; nt < 8; ++nt) o[16 * nt] = acc[nt][jj]; }
;     if (F.tid < 2) ((float*)(F.ws + WS_SMALL))[ch * 4 + 2 * g + F.tid] = __expf(AC[F.tid * 128 + 127]);
	s_nop 3
	s_nop 0
	v_mfma_f32_16x16x32_bf16 v[20:23], v[36:39], v[44:47], v[20:23]
	v_mov_b64_e32 v[46:47], v[42:43]
	ds_read_b128 v[36:39], v0 offset:52352
	v_mov_b64_e32 v[44:45], v[40:41]
	s_waitcnt lgkmcnt(0)
	s_nop 3
	s_nop 0
	v_mfma_f32_16x16x32_bf16 v[24:27], v[36:39], v[44:47], v[24:27]
	v_mov_b64_e32 v[46:47], v[42:43]
	ds_read_b128 v[36:39], v0 offset:56704
	v_mov_b64_e32 v[44:45], v[40:41]
	s_waitcnt lgkmcnt(0)
	s_nop 3
	s_nop 0
	v_mfma_f32_16x16x32_bf16 v[28:31], v[36:39], v[44:47], v[28:31]
	v_mov_b64_e32 v[46:47], v[42:43]
	ds_read_b128 v[36:39], v0 offset:61056
	v_mov_b64_e32 v[44:45], v[40:41]
	s_waitcnt lgkmcnt(0)
	s_nop 3
	s_nop 0
	v_mfma_f32_16x16x32_bf16 v[32:35], v[36:39], v[44:47], v[32:35]
	ds_read_b128 v[36:39], v0 offset:65408
	s_waitcnt lgkmcnt(0)
	s_nop 3
	s_nop 0
	v_mfma_f32_16x16x32_bf16 v[36:39], v[36:39], v[40:43], v[8:11]
	s_nop 2
	ds_read_b128 v[8:11], v0 offset:35008
	ds_read_b128 v[40:43], v48 offset:192
	s_waitcnt lgkmcnt(0)
	v_mov_b64_e32 v[46:47], v[42:43]
	v_mov_b64_e32 v[44:45], v[40:41]
	s_nop 3
	s_nop 1
	v_mfma_f32_16x16x32_bf16 v[4:7], v[8:11], v[44:47], v[4:7]
	v_mov_b64_e32 v[46:47], v[42:43]
	ds_read_b128 v[8:11], v0 offset:39360
	v_mov_b64_e32 v[44:45], v[40:41]
	s_waitcnt lgkmcnt(0)
	s_nop 3
	s_nop 0
	v_mfma_f32_16x16x32_bf16 v[8:11], v[8:11], v[44:47], v[12:15]
	v_mov_b64_e32 v[46:47], v[42:43]
	v_mov_b64_e32 v[44:45], v[40:41]
	s_nop 0
	ds_read_b128 v[12:15], v0 offset:43712
	s_waitcnt lgkmcnt(0)
	s_nop 3
	s_nop 0
	v_mfma_f32_16x16x32_bf16 v[12:15], v[12:15], v[44:47], v[16:19]
	v_mov_b64_e32 v[46:47], v[42:43]
	v_mov_b64_e32 v[44:45], v[40:41]
	s_nop 0
	ds_read_b128 v[16:19], v0 offset:48064
	s_waitcnt lgkmcnt(0)
	s_nop 3
	s_nop 0
	v_mfma_f32_16x16x32_bf16 v[16:19], v[16:19], v[44:47], v[20:23]
	v_mov_b64_e32 v[46:47], v[42:43]
	v_mov_b64_e32 v[44:45], v[40:41]
	s_nop 0
	ds_read_b128 v[20:23], v0 offset:52416
	s_waitcnt lgkmcnt(0)
	s_nop 3
	s_nop 0
	v_mfma_f32_16x16x32_bf16 v[20:23], v[20:23], v[44:47], v[24:27]
	v_mov_b64_e32 v[46:47], v[42:43]
	v_mov_b64_e32 v[44:45], v[40:41]
	s_nop 0
	ds_read_b128 v[24:27], v0 offset:56768
	s_waitcnt lgkmcnt(0)
	s_nop 3
	s_nop 0
	v_mfma_f32_16x16x32_bf16 v[24:27], v[24:27], v[44:47], v[28:31]
	v_mov_b64_e32 v[46:47], v[42:43]
	v_mov_b64_e32 v[44:45], v[40:41]
	s_nop 0
	ds_read_b128 v[28:31], v0 offset:61120
	s_waitcnt lgkmcnt(0)
	s_nop 3
	s_nop 0
	v_mfma_f32_16x16x32_bf16 v[28:31], v[28:31], v[44:47], v[32:35]
	s_nop 2
	ds_read_b128 v[32:35], v0 offset:65472
	s_waitcnt lgkmcnt(0)
	s_nop 3
	v_lshlrev_b32_e32 v0, 7, v133
	v_mfma_f32_16x16x32_bf16 v[32:35], v[32:35], v[40:43], v[36:39]
	s_nop 2
	v_lshl_add_u64 v[36:37], s[0:1], 0, v[2:3]
	s_lshl_b32 s0, s37, 13
	v_mov_b32_e32 v2, s0
	s_movk_i32 s0, 0x7800
	v_bitop3_b32 v2, v0, s0, v2 bitop3:0xc8
	v_lshl_add_u64 v[38:39], v[36:37], 0, v[2:3]
	s_mov_b64 s[0:1], 0x1f100000
	v_lshl_add_u64 v[36:37], v[38:39], 0, s[0:1]
	s_mov_b32 s0, 0x1f100000
	v_add_co_u32_e32 v38, vcc, s0, v38
	s_nop 1
	v_addc_co_u32_e32 v39, vcc, 0, v39, vcc
	v_cmp_gt_i32_e32 vcc, 2, v132
	v_and_b32_e32 v40, 15, v133
	v_lshrrev_b32_e32 v41, 4, v133
	v_mul_u32_u24_e32 v40, 0x1fc, v40
	v_mul_u32_u24_e32 v41, 0x7f0, v41
	v_sub_u32_e32 v40, v40, v41
	v_ashrrev_i32_e32 v41, 31, v40
	v_lshl_add_u64 v[36:37], v[36:37], 0, v[40:41]
	s_nop 7
	global_store_dwordx4 v[36:37], v[4:7], off
	global_store_dwordx4 v[36:37], v[8:11], off offset:64
	global_store_dwordx4 v[36:37], v[12:15], off offset:128
	global_store_dwordx4 v[36:37], v[16:19], off offset:192
	global_store_dwordx4 v[36:37], v[20:23], off offset:256
	global_store_dwordx4 v[36:37], v[24:27], off offset:320
	global_store_dwordx4 v[36:37], v[28:31], off offset:384
	global_store_dwordx4 v[36:37], v[32:35], off offset:448
	s_and_saveexec_b64 s[0:1], vcc
	s_cbranch_execz .LBB0_840
	v_lshl_add_u32 v0, v132, 9, s36
	ds_read_b32 v0, v0 offset:508
	v_add_u32_e32 v4, s2, v132
	v_ashrrev_i32_e32 v5, 31, v4
	v_lshl_add_u64 v[4:5], v[4:5], 2, s[20:21]
	v_add_co_u32_e32 v4, vcc, 0x300000, v4
	s_waitcnt lgkmcnt(0)
	v_mul_f32_e32 v0, 0x3fb8aa3b, v0
	v_exp_f32_e32 v0, v0
	v_addc_co_u32_e32 v5, vcc, 0, v5, vcc
	global_store_dword v[4:5], v0, off
